# four critical-path trims on v65: hgrn_out2 counted wait (state-tile loads waited at first MFMA), attention rescale test moved in front of the tile barrier, gate/up first-unit token-map loads batched,
# baseline (speedup 1.0000x reference)
; #define LAS __attribute__((address_space(3)))
; __device__ __forceinline__ void ph_hgrn_kv2(const P& p, int G, int bid, LAS unsigned char* lds, int tid, int wave) {
;     ...
;       const int t2 = tid_ - 256;
; #pragma unroll
;       for (int i = 0; i < 4; ++i) { const int idx = t2 + 256 * i, r = idx >> 4, ch = idx & 15;
;         *(LAS u32x4*)(VL + r * HG_LDK + ch * 8) = *(const u32x4*)(WSP(bf16_t, WS_PROJ) + (size_t)(rbase + r) * INW + C_HI + h * 128 + ch * 8); }
;     }
.LBB0_315:
	v_mov_b32_e32 v78, v77
	v_readlane_b32 s12, v253, 14
	s_ashr_i32 s2, s17, 2
	s_and_b32 s9, s17, 3
	v_readlane_b32 s13, v253, 15
	v_add_u32_e32 v1, 0x200, v78
	s_lshl_b32 s18, s2, 6
	s_lshl_b32 s24, s9, 7
	s_mov_b64 s[6:7], -1
	s_and_b64 vcc, exec, s[12:13]
	v_ashrrev_i32_e32 v48, 4, v78
	v_ashrrev_i32_e32 v49, 4, v1
	s_cbranch_vccz .LBB0_317
	v_add_u32_e32 v0, 0xffffff00, v78
	v_lshlrev_b32_e32 v2, 4, v78
	v_ashrrev_i32_e32 v0, 4, v0
	v_and_b32_e32 v96, 0xf0, v2
	v_add_u32_e32 v2, s18, v0
	v_mov_b64_e32 v[6:7], s[0:1]
	v_mad_i64_i32 v[2:3], s[6:7], v2, s11, v[6:7]
	s_lshl_b32 s64, s24, 1
	v_lshl_add_u64 v[2:3], v[2:3], 0, s[64:65]
	v_lshl_add_u64 v[2:3], v[2:3], 0, v[96:97]
	v_add_co_u32_e32 v2, vcc, 0x226b5000, v2
	v_add_u32_e32 v8, 0, v96
	s_nop 0
	v_addc_co_u32_e32 v3, vcc, 0, v3, vcc
	s_lshl_b32 s26, s11, 4
	s_mov_b32 s27, 0
	v_lshl_add_u64 v[12:13], v[2:3], 0, s[26:27]
	v_lshl_add_u64 v[14:15], v[12:13], 0, s[26:27]
	v_lshl_add_u64 v[16:17], v[14:15], 0, s[26:27]
	global_load_dwordx4 v[20:23], v[2:3], off
	global_load_dwordx4 v[24:27], v[12:13], off
	global_load_dwordx4 v[28:31], v[14:15], off
	global_load_dwordx4 v[32:35], v[16:17], off
	s_movk_i32 s12, 0x120
	v_mad_u64_u32 v[10:11], s[6:7], v0, s12, v[8:9]
	v_ashrrev_i32_e32 v0, 4, v78
	v_ashrrev_i32_e32 v2, 4, v1
	s_mov_b32 s3, 0x226b5000
	s_ashr_i32 s19, s18, 31
	s_mov_b64 s[6:7], 0
	s_waitcnt vmcnt(0)
	ds_write_b128 v10, v[20:23] offset:36864
	ds_write_b128 v10, v[24:27] offset:41472
	ds_write_b128 v10, v[28:31] offset:46080
	ds_write_b128 v10, v[32:35] offset:50688

; #define SBAR() __builtin_amdgcn_sched_barrier(0)
; __device__ __forceinline__ void finishSM(f32x16& p0, f32x16& p1, float alpha, float& l_reg, bf16x8& pa0, bf16x8& pa1, bf16x8& pa2, bf16x8& pa3) {
;   for (int r = 0; r < 16; ++r) p1[r] = __builtin_amdgcn_exp2f(p1[r]);
;   float ps = 0; for (int r = 0; r < 16; ++r) ps += p0[r]; for (int r = 0; r < 16; ++r) ps += p1[r];
;   { auto rr = __builtin_amdgcn_permlane32_swap(__float_as_uint(ps), __float_as_uint(ps), false, false);
;     ps = __uint_as_float(rr[0]) + __uint_as_float(rr[1]); }
;   l_reg = l_reg * alpha + ps;
;     ...
;   PK4(p0, 0, pa0); PK4(p0, 8, pa1); PK4(p1, 0, pa2); PK4(p1, 8, pa3);
;     ...
; }
; template <bool HALF> __device__ __forceinline__ void qkt(f32x16& p0, f32x16& p1, const char* Ks, const bf16x8* qr, int r32, int hi, int koff) {
;   p0 = f32x16{}; p1 = f32x16{};
;   for (int d0 = 0; d0 < (HALF ? 4 : 8); ++d0) { int cb = (d0 * 16 + hi * 8) * 2 + koff;
;     bf16x8 b0 = *reinterpret_cast<const bf16x8*>(Ks + KSWZ(r32, cb));
;     bf16x8 b1 = *reinterpret_cast<const bf16x8*>(Ks + KSWZ(32 + r32, cb));
;     p0 = __builtin_amdgcn_mfma_f32_32x32x16_bf16(b0, qr[d0], p0, 0, 0, 0);
;     p1 = __builtin_amdgcn_mfma_f32_32x32x16_bf16(b1, qr[d0], p1, 0, 0, 0); }
; }
; __device__ __forceinline__ int v_st(int k, int c) { const int kk = (k & ~0xC) | ((k & 4) << 1) | ((k & 8) >> 1); return ((kk >> 3) * 4 + (c >> 5)) * 512 + ((kk & 7) * 32 + (c & 31)) * 2; }
; __device__ __forceinline__ int v_rd_base(int lane) { return ((lane & 3) << 3) | (((lane >> 2) & 3) << 6) | (((lane >> 4) & 1) << 5) | (((lane >> 5) & 1) << 8); }
; template <int OFF> __device__ __forceinline__ s16x4 tr_read(int vb) {
;   s16x4 r; asm volatile("ds_read_b64_tr_b16 %0, %1 offset:%2" : "=&v"(r) : "v"(vb), "i"(OFF) : "memory"); return r;
; }
; template <int D0> __device__ __forceinline__ void pv_one(f32x16& od, int vb, bf16x8 pa0, bf16x8 pa1, bf16x8 pa2, bf16x8 pa3) {
;   const s16x4 l0 = tr_read<v_rd_off(D0, 0, 0)>(vb), h0 = tr_read<v_rd_off(D0, 0, 1)>(vb), l1 = tr_read<v_rd_off(D0, 1, 0)>(vb), h1 = tr_read<v_rd_off(D0, 1, 1)>(vb);
;   const s16x4 l2 = tr_read<v_rd_off(D0, 2, 0)>(vb), h2 = tr_read<v_rd_off(D0, 2, 1)>(vb), l3 = tr_read<v_rd_off(D0, 3, 0)>(vb), h3 = tr_read<v_rd_off(D0, 3, 1)>(vb);
;   asm volatile("s_waitcnt lgkmcnt(0)" ::: "memory"); SBAR();
;     ...
;   od = __builtin_amdgcn_mfma_f32_32x32x16_bf16(pa0, PK(l0, h0), od, 0, 0, 0);
.Lmv_f:
	v_exp_f32_e32 v158, v158
	v_add_f32_e32 v162, v169, v162
	v_exp_f32_e32 v159, v159
	v_add_f32_e32 v162, v172, v162
	v_exp_f32_e32 v154, v154
	v_add_f32_e32 v162, v160, v162
	v_exp_f32_e32 v155, v155
	s_waitcnt lgkmcnt(0)
	v_mfma_f32_32x32x16_bf16 v[64:79], v[228:231], v[126:129], v[64:79]
	ds_read_b128 v[190:193], v222 offset:49152
	ds_read_b128 v[228:231], v222 offset:57344
	v_add_f32_e32 v162, v161, v162
	v_exp_f32_e32 v150, v150
	v_add_f32_e32 v162, v158, v162
	v_exp_f32_e32 v151, v151
	v_add_f32_e32 v162, v159, v162
	v_exp_f32_e32 v148, v148
	s_waitcnt lgkmcnt(1)
	v_mfma_f32_32x32x16_bf16 v[80:95], v[190:193], v[122:125], v[80:95]
	v_add_f32_e32 v162, v154, v162
	v_exp_f32_e32 v149, v149
	v_add_f32_e32 v162, v155, v162
	v_exp_f32_e32 v156, v156
	v_add_f32_e32 v162, v150, v162
	v_exp_f32_e32 v157, v157
	v_add_f32_e32 v162, v151, v162
	s_waitcnt lgkmcnt(0)
	v_mfma_f32_32x32x16_bf16 v[64:79], v[228:231], v[122:125], v[64:79]
	ds_read_b128 v[190:193], v210 offset:49152
	ds_read_b128 v[228:231], v210 offset:57344
	v_exp_f32_e32 v152, v152
	v_add_f32_e32 v162, v148, v162
	v_exp_f32_e32 v153, v153
	v_add_f32_e32 v162, v149, v162
	v_exp_f32_e32 v146, v146
	v_add_f32_e32 v162, v156, v162
	s_waitcnt lgkmcnt(1)
	v_mfma_f32_32x32x16_bf16 v[80:95], v[190:193], v[114:117], v[80:95]
	v_exp_f32_e32 v147, v147
	v_add_f32_e32 v162, v157, v162
	v_add_f32_e32 v162, v152, v162
	v_add_f32_e32 v162, v153, v162
	v_add_f32_e32 v162, v146, v162
	v_add_f32_e32 v227, v147, v162
	s_waitcnt lgkmcnt(0)
	v_mfma_f32_32x32x16_bf16 v[64:79], v[228:231], v[114:117], v[64:79]
	ds_read_b128 v[190:193], v211 offset:49152
	ds_read_b128 v[228:231], v211 offset:57344
	s_waitcnt lgkmcnt(1)
	v_mfma_f32_32x32x16_bf16 v[80:95], v[190:193], v[110:113], v[80:95]
	s_waitcnt lgkmcnt(0)
	v_mfma_f32_32x32x16_bf16 v[64:79], v[228:231], v[110:113], v[64:79]
	ds_read_b128 v[190:193], v223 offset:49152
	ds_read_b128 v[228:231], v223 offset:57344
	s_waitcnt lgkmcnt(1)
	v_mfma_f32_32x32x16_bf16 v[80:95], v[190:193], v[106:109], v[80:95]
	s_waitcnt lgkmcnt(0)
	v_mfma_f32_32x32x16_bf16 v[64:79], v[228:231], v[106:109], v[64:79]
	ds_read_b128 v[190:193], v225 offset:49152
	ds_read_b128 v[228:231], v225 offset:57344
	s_waitcnt lgkmcnt(1)
	v_mfma_f32_32x32x16_bf16 v[80:95], v[190:193], v[102:105], v[80:95]
	s_waitcnt lgkmcnt(0)
	v_mfma_f32_32x32x16_bf16 v[64:79], v[228:231], v[102:105], v[64:79]
	ds_read_b128 v[190:193], v224 offset:49152
	ds_read_b128 v[228:231], v224 offset:57344
	v_cvt_pk_bf16_f32 v162, v163, v177
	v_cvt_pk_bf16_f32 v163, v164, v188
	v_cvt_pk_bf16_f32 v164, v176, v189
	v_cvt_pk_bf16_f32 v165, v165, v175
	v_cvt_pk_bf16_f32 v166, v166, v173
	v_cvt_pk_bf16_f32 v167, v167, v174
	s_waitcnt lgkmcnt(1)
	v_mfma_f32_32x32x16_bf16 v[80:95], v[190:193], v[98:101], v[80:95]
	v_permlane32_swap_b32_e32 v162, v164
	v_cvt_pk_bf16_f32 v168, v168, v171
	v_cvt_pk_bf16_f32 v169, v169, v172
	v_cvt_pk_bf16_f32 v172, v160, v161
	v_cvt_pk_bf16_f32 v173, v158, v159
	v_cvt_pk_bf16_f32 v174, v154, v155
	s_waitcnt lgkmcnt(0)
	v_mfma_f32_32x32x16_bf16 v[64:79], v[228:231], v[98:101], v[64:79]
	v_mov_b32_e32 v228, v227
	s_nop 1
	v_permlane32_swap_b32_e32 v227, v228
	v_cvt_pk_bf16_f32 v175, v150, v151
	v_cvt_pk_bf16_f32 v230, v148, v149
	v_cvt_pk_bf16_f32 v231, v156, v157
	v_cvt_pk_bf16_f32 v232, v152, v153
	v_cvt_pk_bf16_f32 v233, v146, v147
	v_permlane32_swap_b32_e32 v163, v165
	v_permlane32_swap_b32_e32 v166, v168
	v_permlane32_swap_b32_e32 v167, v169
	v_permlane32_swap_b32_e32 v172, v174
	v_permlane32_swap_b32_e32 v173, v175
	v_permlane32_swap_b32_e32 v230, v232
	v_permlane32_swap_b32_e32 v231, v233
	ds_read_b64_tr_b16 v[234:235], v204 offset:0
	ds_read_b64_tr_b16 v[236:237], v204 offset:0x800
	ds_read_b64_tr_b16 v[238:239], v204 offset:0x1000
	ds_read_b64_tr_b16 v[240:241], v204 offset:0x1800
	ds_read_b64_tr_b16 v[242:243], v204 offset:0x2000
	ds_read_b64_tr_b16 v[244:245], v204 offset:0x2800
	ds_read_b64_tr_b16 v[246:247], v204 offset:0x3000
	ds_read_b64_tr_b16 v[248:249], v204 offset:0x3800
	s_waitcnt lgkmcnt(0)
	s_nop 0
	v_mfma_f32_32x32x16_bf16 v[0:15], v[162:165], v[234:237], v[0:15]
	ds_read_b64_tr_b16 v[234:235], v204 offset:0x200
	ds_read_b64_tr_b16 v[236:237], v204 offset:0xa00
	v_mfma_f32_32x32x16_bf16 v[0:15], v[166:169], v[238:241], v[0:15]
	ds_read_b64_tr_b16 v[238:239], v204 offset:0x1200
	ds_read_b64_tr_b16 v[240:241], v204 offset:0x1a00
	v_mfma_f32_32x32x16_bf16 v[0:15], v[172:175], v[242:245], v[0:15]
	ds_read_b64_tr_b16 v[242:243], v204 offset:0x2200
	ds_read_b64_tr_b16 v[244:245], v204 offset:0x2a00
	v_mfma_f32_32x32x16_bf16 v[0:15], v[230:233], v[246:249], v[0:15]
	ds_read_b64_tr_b16 v[246:247], v204 offset:0x3200
	ds_read_b64_tr_b16 v[248:249], v204 offset:0x3a00
	s_waitcnt lgkmcnt(0)
; __device__ __forceinline__ void partialSM(f32x16& p0, f32x16& p1, float& m_reg, float& mn, float& alpha) {
;   constexpr float C = SCALE * 1.4426950408889634f;
;   float pmax = p0[0]; for (int r = 1; r < 16; ++r) pmax = fmaxf(pmax, p0[r]); for (int r = 0; r < 16; ++r) pmax = fmaxf(pmax, p1[r]);
;   { auto rr = __builtin_amdgcn_permlane32_swap(__float_as_uint(pmax), __float_as_uint(pmax), false, false);
;     pmax = fmaxf(__uint_as_float(rr[0]), __uint_as_float(rr[1])); }
;   if (__builtin_expect(__all(pmax - m_reg <= THR / SCALE), 1)) { mn = m_reg; alpha = 1.f; }
;   else { mn = fmaxf(m_reg, pmax); alpha = __builtin_amdgcn_exp2f((m_reg - mn) * C); m_reg = mn; }
;   float mnC = -mn * C;
;   for (int r = 0; r < 16; ++r) p0[r] = fmaf(p0[r], C, mnC); for (int r = 0; r < 16; ++r) p1[r] = fmaf(p1[r], C, mnC);
;   for (int r = 0; r < 16; ++r) p0[r] = __builtin_amdgcn_exp2f(p0[r]);
; }
; __device__ __forceinline__ void finishSM(f32x16& p0, f32x16& p1, float alpha, float& l_reg, bf16x8& pa0, bf16x8& pa1, bf16x8& pa2, bf16x8& pa3) {
;   for (int r = 0; r < 16; ++r) p1[r] = __builtin_amdgcn_exp2f(p1[r]);
;   float ps = 0; for (int r = 0; r < 16; ++r) ps += p0[r]; for (int r = 0; r < 16; ++r) ps += p1[r];
;   { auto rr = __builtin_amdgcn_permlane32_swap(__float_as_uint(ps), __float_as_uint(ps), false, false);
;     ps = __uint_as_float(rr[0]) + __uint_as_float(rr[1]); }
;   l_reg = l_reg * alpha + ps;
;     ...
;   PK4(p0, 0, pa0); PK4(p0, 8, pa1); PK4(p1, 0, pa2); PK4(p1, 8, pa3);
;     ...
; }
; template <bool HALF> __device__ __forceinline__ void qkt(f32x16& p0, f32x16& p1, const char* Ks, const bf16x8* qr, int r32, int hi, int koff) {
;   p0 = f32x16{}; p1 = f32x16{};
;   for (int d0 = 0; d0 < (HALF ? 4 : 8); ++d0) { int cb = (d0 * 16 + hi * 8) * 2 + koff;
;     bf16x8 b0 = *reinterpret_cast<const bf16x8*>(Ks + KSWZ(r32, cb));
;     bf16x8 b1 = *reinterpret_cast<const bf16x8*>(Ks + KSWZ(32 + r32, cb));
;     p0 = __builtin_amdgcn_mfma_f32_32x32x16_bf16(b0, qr[d0], p0, 0, 0, 0);
;     p1 = __builtin_amdgcn_mfma_f32_32x32x16_bf16(b1, qr[d0], p1, 0, 0, 0); }
; }
; __device__ __forceinline__ int v_st(int k, int c) { const int kk = (k & ~0xC) | ((k & 4) << 1) | ((k & 8) >> 1); return ((kk >> 3) * 4 + (c >> 5)) * 512 + ((kk & 7) * 32 + (c & 31)) * 2; }
	v_mfma_f32_32x32x16_bf16 v[48:63], v[162:165], v[234:237], v[48:63]
	ds_read_b64_tr_b16 v[234:235], v204 offset:0x400
	ds_read_b64_tr_b16 v[236:237], v204 offset:0xc00
	v_mfma_f32_32x32x16_bf16 v[48:63], v[166:169], v[238:241], v[48:63]
	ds_read_b64_tr_b16 v[238:239], v204 offset:0x1400
	ds_read_b64_tr_b16 v[240:241], v204 offset:0x1c00
	v_mfma_f32_32x32x16_bf16 v[48:63], v[172:175], v[242:245], v[48:63]
	ds_read_b64_tr_b16 v[242:243], v204 offset:0x2400
	ds_read_b64_tr_b16 v[244:245], v204 offset:0x2c00
	v_mfma_f32_32x32x16_bf16 v[48:63], v[230:233], v[246:249], v[48:63]
	ds_read_b64_tr_b16 v[246:247], v204 offset:0x3400
	ds_read_b64_tr_b16 v[248:249], v204 offset:0x3c00
	s_waitcnt lgkmcnt(0)
	v_mfma_f32_32x32x16_bf16 v[32:47], v[162:165], v[234:237], v[32:47]
	ds_read_b64_tr_b16 v[234:235], v204 offset:0x600
	ds_read_b64_tr_b16 v[236:237], v204 offset:0xe00
	v_mfma_f32_32x32x16_bf16 v[32:47], v[166:169], v[238:241], v[32:47]
	ds_read_b64_tr_b16 v[238:239], v204 offset:0x1600
	ds_read_b64_tr_b16 v[240:241], v204 offset:0x1e00
	v_mfma_f32_32x32x16_bf16 v[32:47], v[172:175], v[242:245], v[32:47]
	ds_read_b64_tr_b16 v[242:243], v204 offset:0x2600
	ds_read_b64_tr_b16 v[244:245], v204 offset:0x2e00
	v_mfma_f32_32x32x16_bf16 v[32:47], v[230:233], v[246:249], v[32:47]
	ds_read_b64_tr_b16 v[246:247], v204 offset:0x3600
	ds_read_b64_tr_b16 v[248:249], v204 offset:0x3e00
	s_waitcnt lgkmcnt(0)
	v_mfma_f32_32x32x16_bf16 v[16:31], v[162:165], v[234:237], v[16:31]
	v_max_f32_e32 v162, v81, v81
	v_max_f32_e32 v163, v80, v80
	v_max_f32_e32 v162, v163, v162
	v_max3_f32 v162, v162, v82, v83
	v_max3_f32 v162, v162, v84, v85
	v_max3_f32 v162, v162, v86, v87
	v_max3_f32 v162, v162, v88, v89
	v_max3_f32 v162, v162, v90, v91
	v_max3_f32 v162, v162, v92, v93
	v_mfma_f32_32x32x16_bf16 v[16:31], v[166:169], v[238:241], v[16:31]
	v_max3_f32 v162, v162, v94, v95
	v_max3_f32 v162, v162, v64, v65
	v_max3_f32 v162, v162, v66, v67
	v_max3_f32 v162, v162, v68, v69
	v_max3_f32 v162, v162, v70, v71
	v_max3_f32 v162, v162, v72, v73
	v_max3_f32 v162, v162, v74, v75
	v_max3_f32 v162, v162, v76, v77
	v_mfma_f32_32x32x16_bf16 v[16:31], v[172:175], v[242:245], v[16:31]
	v_max3_f32 v162, v162, v78, v79
	v_mov_b32_e32 v163, v162
	s_nop 1
	v_permlane32_swap_b32_e32 v162, v163
	v_max_f32_e32 v163, v163, v163
	v_max_f32_e32 v162, v162, v162
	v_max_f32_e32 v162, v162, v163
	v_sub_f32_e32 v163, v162, v170
	v_cmp_ge_f32_e32 vcc, s87, v163
	v_max_f32_e32 v163, v170, v170
	v_max_f32_e32 v162, v163, v162
	v_mfma_f32_32x32x16_bf16 v[16:31], v[230:233], v[246:249], v[16:31]
	v_sub_f32_e32 v163, v170, v162
	v_mul_f32_e32 v163, 0x3e0293ee, v163
	v_exp_f32_e32 v163, v163
	s_cmp_eq_u64 vcc, exec
	s_cselect_b64 s[42:43], -1, 0
	v_cndmask_b32_e64 v229, v163, 1.0, s[42:43]
	v_cmp_gt_f32_e32 vcc, 1.0, v229
	s_waitcnt vmcnt(0)
	s_barrier
	s_cbranch_vccz .LBB0_429
	s_and_saveexec_b64 s[6:7], s[40:41]
	ds_write_b32 v201, v229 offset:128
	s_or_b64 exec, exec, s[6:7]
	s_waitcnt lgkmcnt(0)
	v_add_u32_e32 v163, v200, v96
	ds_read_b128 v[164:167], v163 offset:224
	ds_read_b128 v[172:175], v163 offset:192
	ds_read_b128 v[230:233], v163 offset:160
	ds_read_b128 v[234:237], v163 offset:128
	s_waitcnt lgkmcnt(3)
	v_pk_mul_f32 v[12:13], v[12:13], v[164:165]
	s_waitcnt lgkmcnt(2)
	v_pk_mul_f32 v[8:9], v[8:9], v[172:173]
	s_waitcnt lgkmcnt(1)
	v_pk_mul_f32 v[4:5], v[4:5], v[230:231]
	v_pk_mul_f32 v[14:15], v[14:15], v[166:167]
	v_pk_mul_f32 v[10:11], v[10:11], v[174:175]
	v_pk_mul_f32 v[6:7], v[6:7], v[232:233]
	s_waitcnt lgkmcnt(0)
	v_pk_mul_f32 v[2:3], v[2:3], v[236:237]
	v_pk_mul_f32 v[0:1], v[0:1], v[234:235]
	v_pk_mul_f32 v[60:61], v[60:61], v[164:165]
	v_pk_mul_f32 v[56:57], v[56:57], v[172:173]
	v_pk_mul_f32 v[52:53], v[52:53], v[230:231]
	v_pk_mul_f32 v[62:63], v[62:63], v[166:167]
	v_pk_mul_f32 v[58:59], v[58:59], v[174:175]
	v_pk_mul_f32 v[54:55], v[54:55], v[232:233]
	v_pk_mul_f32 v[50:51], v[50:51], v[236:237]
	v_pk_mul_f32 v[48:49], v[48:49], v[234:235]
	v_pk_mul_f32 v[44:45], v[44:45], v[164:165]
	v_pk_mul_f32 v[40:41], v[40:41], v[172:173]
	v_pk_mul_f32 v[36:37], v[36:37], v[230:231]
	v_pk_mul_f32 v[46:47], v[46:47], v[166:167]
	v_pk_mul_f32 v[42:43], v[42:43], v[174:175]
	v_pk_mul_f32 v[38:39], v[38:39], v[232:233]
	v_pk_mul_f32 v[34:35], v[34:35], v[236:237]
	v_pk_mul_f32 v[32:33], v[32:33], v[234:235]
	v_pk_mul_f32 v[28:29], v[28:29], v[164:165]
	v_pk_mul_f32 v[24:25], v[24:25], v[172:173]
	v_pk_mul_f32 v[20:21], v[20:21], v[230:231]
	v_pk_mul_f32 v[30:31], v[30:31], v[166:167]
	v_pk_mul_f32 v[26:27], v[26:27], v[174:175]
	v_pk_mul_f32 v[22:23], v[22:23], v[232:233]
	v_pk_mul_f32 v[18:19], v[18:19], v[236:237]
	v_pk_mul_f32 v[16:17], v[16:17], v[234:235]

; __device__ __forceinline__ void partialSM(f32x16& p0, f32x16& p1, float& m_reg, float& mn, float& alpha) {
;   constexpr float C = SCALE * 1.4426950408889634f;
;   float pmax = p0[0]; for (int r = 1; r < 16; ++r) pmax = fmaxf(pmax, p0[r]); for (int r = 0; r < 16; ++r) pmax = fmaxf(pmax, p1[r]);
;   { auto rr = __builtin_amdgcn_permlane32_swap(__float_as_uint(pmax), __float_as_uint(pmax), false, false);
;     pmax = fmaxf(__uint_as_float(rr[0]), __uint_as_float(rr[1])); }
;   if (__builtin_expect(__all(pmax - m_reg <= THR / SCALE), 1)) { mn = m_reg; alpha = 1.f; }
;   else { mn = fmaxf(m_reg, pmax); alpha = __builtin_amdgcn_exp2f((m_reg - mn) * C); m_reg = mn; }
;   float mnC = -mn * C;
;   for (int r = 0; r < 16; ++r) p0[r] = fmaf(p0[r], C, mnC); for (int r = 0; r < 16; ++r) p1[r] = fmaf(p1[r], C, mnC);
;   for (int r = 0; r < 16; ++r) p0[r] = __builtin_amdgcn_exp2f(p0[r]);
; }
; __device__ __forceinline__ void finishSM(f32x16& p0, f32x16& p1, float alpha, float& l_reg, bf16x8& pa0, bf16x8& pa1, bf16x8& pa2, bf16x8& pa3) {
;   for (int r = 0; r < 16; ++r) p1[r] = __builtin_amdgcn_exp2f(p1[r]);
;   float ps = 0; for (int r = 0; r < 16; ++r) ps += p0[r]; for (int r = 0; r < 16; ++r) ps += p1[r];
;   { auto rr = __builtin_amdgcn_permlane32_swap(__float_as_uint(ps), __float_as_uint(ps), false, false);
;     ps = __uint_as_float(rr[0]) + __uint_as_float(rr[1]); }
;   l_reg = l_reg * alpha + ps;
;     ...
;   PK4(p0, 0, pa0); PK4(p0, 8, pa1); PK4(p1, 0, pa2); PK4(p1, 8, pa3);
;     ...
; }
; template <bool HALF> __device__ __forceinline__ void qkt(f32x16& p0, f32x16& p1, const char* Ks, const bf16x8* qr, int r32, int hi, int koff) {
;   p0 = f32x16{}; p1 = f32x16{};
;   for (int d0 = 0; d0 < (HALF ? 4 : 8); ++d0) { int cb = (d0 * 16 + hi * 8) * 2 + koff;
;     bf16x8 b0 = *reinterpret_cast<const bf16x8*>(Ks + KSWZ(r32, cb));
;     bf16x8 b1 = *reinterpret_cast<const bf16x8*>(Ks + KSWZ(32 + r32, cb));
;     p0 = __builtin_amdgcn_mfma_f32_32x32x16_bf16(b0, qr[d0], p0, 0, 0, 0);
;     p1 = __builtin_amdgcn_mfma_f32_32x32x16_bf16(b1, qr[d0], p1, 0, 0, 0); }
; }
; __device__ __forceinline__ int v_st(int k, int c) { const int kk = (k & ~0xC) | ((k & 4) << 1) | ((k & 8) >> 1); return ((kk >> 3) * 4 + (c >> 5)) * 512 + ((kk & 7) * 32 + (c & 31)) * 2; }
.LBB0_431:
	ds_read_b64_tr_b16 v[188:189], v203 offset:0
	ds_read_b64_tr_b16 v[190:191], v203 offset:0x800
	ds_read_b64_tr_b16 v[192:193], v203 offset:0x1000
	ds_read_b64_tr_b16 v[194:195], v203 offset:0x1800
	ds_read_b64_tr_b16 v[212:213], v203 offset:0x2000
	ds_read_b64_tr_b16 v[214:215], v203 offset:0x2800
	ds_read_b64_tr_b16 v[234:235], v203 offset:0x3000
	ds_read_b64_tr_b16 v[236:237], v203 offset:0x3800
	s_waitcnt lgkmcnt(0)
	s_nop 0
	v_mfma_f32_32x32x16_bf16 v[0:15], v[162:165], v[188:191], v[0:15]
	ds_read_b64_tr_b16 v[188:189], v203 offset:0x200
	ds_read_b64_tr_b16 v[190:191], v203 offset:0xa00
	v_mfma_f32_32x32x16_bf16 v[0:15], v[166:169], v[192:195], v[0:15]
	ds_read_b64_tr_b16 v[192:193], v203 offset:0x1200
	ds_read_b64_tr_b16 v[194:195], v203 offset:0x1a00
	v_mfma_f32_32x32x16_bf16 v[0:15], v[170:173], v[212:215], v[0:15]
	ds_read_b64_tr_b16 v[212:213], v203 offset:0x2200
	ds_read_b64_tr_b16 v[214:215], v203 offset:0x2a00
	v_mfma_f32_32x32x16_bf16 v[0:15], v[174:177], v[234:237], v[0:15]
	ds_read_b64_tr_b16 v[234:235], v203 offset:0x3200
	ds_read_b64_tr_b16 v[236:237], v203 offset:0x3a00
	s_waitcnt lgkmcnt(0)
	v_mfma_f32_32x32x16_bf16 v[48:63], v[162:165], v[188:191], v[48:63]
	ds_read_b64_tr_b16 v[188:189], v203 offset:0x400
	ds_read_b64_tr_b16 v[190:191], v203 offset:0xc00
	v_mfma_f32_32x32x16_bf16 v[48:63], v[166:169], v[192:195], v[48:63]
	ds_read_b64_tr_b16 v[192:193], v203 offset:0x1400
	ds_read_b64_tr_b16 v[194:195], v203 offset:0x1c00
	v_mfma_f32_32x32x16_bf16 v[48:63], v[170:173], v[212:215], v[48:63]
	ds_read_b64_tr_b16 v[212:213], v203 offset:0x2400
	ds_read_b64_tr_b16 v[214:215], v203 offset:0x2c00
	v_mfma_f32_32x32x16_bf16 v[48:63], v[174:177], v[234:237], v[48:63]
	ds_read_b64_tr_b16 v[234:235], v203 offset:0x3400
	ds_read_b64_tr_b16 v[236:237], v203 offset:0x3c00
	s_waitcnt lgkmcnt(0)
	v_mfma_f32_32x32x16_bf16 v[32:47], v[162:165], v[188:191], v[32:47]
	ds_read_b64_tr_b16 v[188:189], v203 offset:0x600
	ds_read_b64_tr_b16 v[190:191], v203 offset:0xe00
	v_mfma_f32_32x32x16_bf16 v[32:47], v[166:169], v[192:195], v[32:47]
	ds_read_b64_tr_b16 v[192:193], v203 offset:0x1600
	ds_read_b64_tr_b16 v[194:195], v203 offset:0x1e00
	v_mfma_f32_32x32x16_bf16 v[32:47], v[170:173], v[212:215], v[32:47]
	ds_read_b64_tr_b16 v[212:213], v203 offset:0x2600
	ds_read_b64_tr_b16 v[214:215], v203 offset:0x2e00
	v_mfma_f32_32x32x16_bf16 v[32:47], v[174:177], v[234:237], v[32:47]
	ds_read_b64_tr_b16 v[234:235], v203 offset:0x3600
	ds_read_b64_tr_b16 v[236:237], v203 offset:0x3e00
	s_waitcnt lgkmcnt(0)
	v_mfma_f32_32x32x16_bf16 v[16:31], v[162:165], v[188:191], v[16:31]
	v_max_f32_e32 v162, v81, v81
	v_max_f32_e32 v163, v80, v80
	v_max_f32_e32 v162, v163, v162
	v_max3_f32 v162, v162, v82, v83
	v_max3_f32 v162, v162, v84, v85
	v_max3_f32 v162, v162, v86, v87
	v_max3_f32 v162, v162, v88, v89
	v_max3_f32 v162, v162, v90, v91
	v_max3_f32 v162, v162, v92, v93
	v_mfma_f32_32x32x16_bf16 v[16:31], v[166:169], v[192:195], v[16:31]
	v_max3_f32 v162, v162, v94, v95
	v_max3_f32 v162, v162, v64, v65
	v_max3_f32 v162, v162, v66, v67
	v_max3_f32 v162, v162, v68, v69
	v_max3_f32 v162, v162, v70, v71
	v_max3_f32 v162, v162, v72, v73
	v_max3_f32 v162, v162, v74, v75
	v_max3_f32 v162, v162, v76, v77
	v_mfma_f32_32x32x16_bf16 v[16:31], v[170:173], v[212:215], v[16:31]
	v_max3_f32 v162, v162, v78, v79
	v_mov_b32_e32 v163, v162
	s_nop 1
	v_permlane32_swap_b32_e32 v162, v163
	v_max_f32_e32 v163, v163, v163
	v_max_f32_e32 v162, v162, v162
	v_max_f32_e32 v162, v162, v163
	v_sub_f32_e32 v163, v162, v230
	v_cmp_ge_f32_e32 vcc, s87, v163
	v_max_f32_e32 v163, v230, v230
	v_max_f32_e32 v163, v163, v162
	v_mfma_f32_32x32x16_bf16 v[16:31], v[174:177], v[234:237], v[16:31]
	v_sub_f32_e32 v162, v230, v163
	v_mul_f32_e32 v162, 0x3e0293ee, v162
	v_exp_f32_e32 v162, v162
	s_cmp_eq_u64 vcc, exec
	s_cselect_b64 s[42:43], -1, 0
	v_cndmask_b32_e64 v162, v162, 1.0, s[42:43]
	v_cmp_gt_f32_e32 vcc, 1.0, v162
	s_waitcnt vmcnt(0)
	s_barrier
	s_mov_b32 s54, 1
	s_cbranch_vccz .LBB0_435
	s_and_saveexec_b64 s[6:7], s[40:41]
	ds_write_b32 v201, v162 offset:128
	s_or_b64 exec, exec, s[6:7]
	s_waitcnt lgkmcnt(0)
	v_add_u32_e32 v158, v200, v96
	ds_read_b128 v[146:149], v158 offset:224
	ds_read_b128 v[150:153], v158 offset:192
	ds_read_b128 v[154:157], v158 offset:160
	ds_read_b128 v[158:161], v158 offset:128
	s_waitcnt lgkmcnt(3)
	v_pk_mul_f32 v[12:13], v[12:13], v[146:147]
	s_waitcnt lgkmcnt(2)
	v_pk_mul_f32 v[8:9], v[8:9], v[150:151]
	s_waitcnt lgkmcnt(1)
	v_pk_mul_f32 v[4:5], v[4:5], v[154:155]
	v_pk_mul_f32 v[14:15], v[14:15], v[148:149]
	v_pk_mul_f32 v[10:11], v[10:11], v[152:153]
	v_pk_mul_f32 v[6:7], v[6:7], v[156:157]
	s_waitcnt lgkmcnt(0)
	v_pk_mul_f32 v[2:3], v[2:3], v[160:161]
	v_pk_mul_f32 v[0:1], v[0:1], v[158:159]
	v_pk_mul_f32 v[60:61], v[60:61], v[146:147]
	v_pk_mul_f32 v[56:57], v[56:57], v[150:151]
	v_pk_mul_f32 v[52:53], v[52:53], v[154:155]
	v_pk_mul_f32 v[62:63], v[62:63], v[148:149]
	v_pk_mul_f32 v[58:59], v[58:59], v[152:153]
	v_pk_mul_f32 v[54:55], v[54:55], v[156:157]
	v_pk_mul_f32 v[50:51], v[50:51], v[160:161]
	v_pk_mul_f32 v[48:49], v[48:49], v[158:159]
	v_pk_mul_f32 v[44:45], v[44:45], v[146:147]
	v_pk_mul_f32 v[40:41], v[40:41], v[150:151]
	v_pk_mul_f32 v[36:37], v[36:37], v[154:155]
	v_pk_mul_f32 v[46:47], v[46:47], v[148:149]
	v_pk_mul_f32 v[42:43], v[42:43], v[152:153]
	v_pk_mul_f32 v[38:39], v[38:39], v[156:157]
	v_pk_mul_f32 v[34:35], v[34:35], v[160:161]
	v_pk_mul_f32 v[32:33], v[32:33], v[158:159]
	v_pk_mul_f32 v[28:29], v[28:29], v[146:147]
	v_pk_mul_f32 v[24:25], v[24:25], v[150:151]
	v_pk_mul_f32 v[20:21], v[20:21], v[154:155]
	v_pk_mul_f32 v[30:31], v[30:31], v[148:149]
	v_pk_mul_f32 v[26:27], v[26:27], v[152:153]
	v_pk_mul_f32 v[22:23], v[22:23], v[156:157]
	v_pk_mul_f32 v[18:19], v[18:19], v[160:161]
	v_pk_mul_f32 v[16:17], v[16:17], v[158:159]

; __device__ __forceinline__ void partialSM(f32x16& p0, f32x16& p1, float& m_reg, float& mn, float& alpha) {
;   constexpr float C = SCALE * 1.4426950408889634f;
;   float pmax = p0[0]; for (int r = 1; r < 16; ++r) pmax = fmaxf(pmax, p0[r]); for (int r = 0; r < 16; ++r) pmax = fmaxf(pmax, p1[r]);
;   { auto rr = __builtin_amdgcn_permlane32_swap(__float_as_uint(pmax), __float_as_uint(pmax), false, false);
;     pmax = fmaxf(__uint_as_float(rr[0]), __uint_as_float(rr[1])); }
;   if (__builtin_expect(__all(pmax - m_reg <= THR / SCALE), 1)) { mn = m_reg; alpha = 1.f; }
;   else { mn = fmaxf(m_reg, pmax); alpha = __builtin_amdgcn_exp2f((m_reg - mn) * C); m_reg = mn; }
;   float mnC = -mn * C;
;   for (int r = 0; r < 16; ++r) p0[r] = fmaf(p0[r], C, mnC); for (int r = 0; r < 16; ++r) p1[r] = fmaf(p1[r], C, mnC);
;   for (int r = 0; r < 16; ++r) p0[r] = __builtin_amdgcn_exp2f(p0[r]);
; }
; __device__ __forceinline__ void finishSM(f32x16& p0, f32x16& p1, float alpha, float& l_reg, bf16x8& pa0, bf16x8& pa1, bf16x8& pa2, bf16x8& pa3) {
;   for (int r = 0; r < 16; ++r) p1[r] = __builtin_amdgcn_exp2f(p1[r]);
;   float ps = 0; for (int r = 0; r < 16; ++r) ps += p0[r]; for (int r = 0; r < 16; ++r) ps += p1[r];
;   { auto rr = __builtin_amdgcn_permlane32_swap(__float_as_uint(ps), __float_as_uint(ps), false, false);
;     ps = __uint_as_float(rr[0]) + __uint_as_float(rr[1]); }
;   l_reg = l_reg * alpha + ps;
;     ...
;   PK4(p0, 0, pa0); PK4(p0, 8, pa1); PK4(p1, 0, pa2); PK4(p1, 8, pa3);
;     ...
; }
; template <bool HALF> __device__ __forceinline__ void qkt(f32x16& p0, f32x16& p1, const char* Ks, const bf16x8* qr, int r32, int hi, int koff) {
;   p0 = f32x16{}; p1 = f32x16{};
;   for (int d0 = 0; d0 < (HALF ? 4 : 8); ++d0) { int cb = (d0 * 16 + hi * 8) * 2 + koff;
;     bf16x8 b0 = *reinterpret_cast<const bf16x8*>(Ks + KSWZ(r32, cb));
;     bf16x8 b1 = *reinterpret_cast<const bf16x8*>(Ks + KSWZ(32 + r32, cb));
;     p0 = __builtin_amdgcn_mfma_f32_32x32x16_bf16(b0, qr[d0], p0, 0, 0, 0);
;     p1 = __builtin_amdgcn_mfma_f32_32x32x16_bf16(b1, qr[d0], p1, 0, 0, 0); }
; }
; __device__ __forceinline__ int v_st(int k, int c) { const int kk = (k & ~0xC) | ((k & 4) << 1) | ((k & 8) >> 1); return ((kk >> 3) * 4 + (c >> 5)) * 512 + ((kk & 7) * 32 + (c & 31)) * 2; }
.Lmv_h:
	v_exp_f32_e32 v142, v142
	v_add_f32_e32 v146, v154, v146
	v_exp_f32_e32 v143, v143
	v_add_f32_e32 v146, v158, v146
	v_exp_f32_e32 v138, v138
	v_add_f32_e32 v146, v144, v146
	v_exp_f32_e32 v139, v139
	s_waitcnt lgkmcnt(0)
	v_mfma_f32_32x32x16_bf16 v[64:79], v[198:201], v[106:109], v[64:79]
	ds_read_b128 v[172:175], v195 offset:49152
	ds_read_b128 v[198:201], v195 offset:57344
	v_add_f32_e32 v146, v145, v146
	v_exp_f32_e32 v134, v134
	v_add_f32_e32 v146, v142, v146
	v_exp_f32_e32 v135, v135
	v_add_f32_e32 v146, v143, v146
	v_exp_f32_e32 v132, v132
	s_waitcnt lgkmcnt(1)
	v_mfma_f32_32x32x16_bf16 v[80:95], v[172:175], v[110:113], v[80:95]
	v_add_f32_e32 v146, v138, v146
	v_exp_f32_e32 v133, v133
	v_add_f32_e32 v146, v139, v146
	v_exp_f32_e32 v140, v140
	v_add_f32_e32 v146, v134, v146
	v_exp_f32_e32 v141, v141
	v_add_f32_e32 v146, v135, v146
	s_waitcnt lgkmcnt(0)
	v_mfma_f32_32x32x16_bf16 v[64:79], v[198:201], v[110:113], v[64:79]
	ds_read_b128 v[172:175], v194 offset:49152
	ds_read_b128 v[198:201], v194 offset:57344
	v_exp_f32_e32 v136, v136
	v_add_f32_e32 v146, v132, v146
	v_exp_f32_e32 v137, v137
	v_add_f32_e32 v146, v133, v146
	v_exp_f32_e32 v130, v130
	v_add_f32_e32 v146, v140, v146
	s_waitcnt lgkmcnt(1)
	v_mfma_f32_32x32x16_bf16 v[80:95], v[172:175], v[102:105], v[80:95]
	v_exp_f32_e32 v131, v131
	v_add_f32_e32 v146, v141, v146
	v_add_f32_e32 v146, v136, v146
	v_add_f32_e32 v146, v137, v146
	v_add_f32_e32 v146, v130, v146
	s_waitcnt lgkmcnt(0)
	v_mfma_f32_32x32x16_bf16 v[64:79], v[198:201], v[102:105], v[64:79]
	v_add_f32_e32 v198, v131, v146
	v_mov_b32_e32 v199, v198
	v_cvt_pk_bf16_f32 v146, v147, v160
	v_cvt_pk_bf16_f32 v147, v148, v161
	v_cvt_pk_bf16_f32 v148, v149, v170
	v_cvt_pk_bf16_f32 v149, v159, v171
	v_cvt_pk_bf16_f32 v200, v151, v155
	v_cvt_pk_bf16_f32 v201, v152, v156
	v_cvt_pk_bf16_f32 v202, v153, v157
	s_nop 1
	v_permlane32_swap_b32_e32 v198, v199
	v_permlane32_swap_b32_e32 v146, v148
	v_cvt_pk_bf16_f32 v203, v154, v158
	v_permlane32_swap_b32_e32 v200, v202
	v_cvt_pk_bf16_f32 v152, v144, v145
	v_cvt_pk_bf16_f32 v153, v142, v143
	v_cvt_pk_bf16_f32 v154, v138, v139
	v_cvt_pk_bf16_f32 v155, v134, v135
	v_cvt_pk_bf16_f32 v156, v132, v133
	v_cvt_pk_bf16_f32 v157, v140, v141
	v_cvt_pk_bf16_f32 v158, v136, v137
	v_cvt_pk_bf16_f32 v159, v130, v131
	v_permlane32_swap_b32_e32 v147, v149
	v_permlane32_swap_b32_e32 v201, v203
	v_permlane32_swap_b32_e32 v152, v154
	v_permlane32_swap_b32_e32 v153, v155
	v_permlane32_swap_b32_e32 v156, v158
	v_permlane32_swap_b32_e32 v157, v159
	ds_read_b64_tr_b16 v[204:205], v187 offset:0
	ds_read_b64_tr_b16 v[206:207], v187 offset:0x800
	ds_read_b64_tr_b16 v[208:209], v187 offset:0x1000
	ds_read_b64_tr_b16 v[210:211], v187 offset:0x1800
	ds_read_b64_tr_b16 v[212:213], v187 offset:0x2000
	ds_read_b64_tr_b16 v[214:215], v187 offset:0x2800
	ds_read_b64_tr_b16 v[222:223], v187 offset:0x3000
	ds_read_b64_tr_b16 v[224:225], v187 offset:0x3800
	s_waitcnt lgkmcnt(0)
	s_nop 0
	v_mfma_f32_32x32x16_bf16 v[0:15], v[146:149], v[204:207], v[0:15]
	ds_read_b64_tr_b16 v[204:205], v187 offset:0x200
	ds_read_b64_tr_b16 v[206:207], v187 offset:0xa00
	v_mfma_f32_32x32x16_bf16 v[0:15], v[200:203], v[208:211], v[0:15]
	ds_read_b64_tr_b16 v[208:209], v187 offset:0x1200
	ds_read_b64_tr_b16 v[210:211], v187 offset:0x1a00
	v_mfma_f32_32x32x16_bf16 v[0:15], v[152:155], v[212:215], v[0:15]
	ds_read_b64_tr_b16 v[212:213], v187 offset:0x2200
	ds_read_b64_tr_b16 v[214:215], v187 offset:0x2a00
	v_mfma_f32_32x32x16_bf16 v[0:15], v[156:159], v[222:225], v[0:15]
	ds_read_b64_tr_b16 v[222:223], v187 offset:0x3200
	ds_read_b64_tr_b16 v[224:225], v187 offset:0x3a00
	s_waitcnt lgkmcnt(0)
	v_mfma_f32_32x32x16_bf16 v[48:63], v[146:149], v[204:207], v[48:63]
	ds_read_b64_tr_b16 v[204:205], v187 offset:0x400
	ds_read_b64_tr_b16 v[206:207], v187 offset:0xc00
	v_mfma_f32_32x32x16_bf16 v[48:63], v[200:203], v[208:211], v[48:63]
	ds_read_b64_tr_b16 v[208:209], v187 offset:0x1400
	ds_read_b64_tr_b16 v[210:211], v187 offset:0x1c00
	v_mfma_f32_32x32x16_bf16 v[48:63], v[152:155], v[212:215], v[48:63]
	ds_read_b64_tr_b16 v[212:213], v187 offset:0x2400
	ds_read_b64_tr_b16 v[214:215], v187 offset:0x2c00
	v_mfma_f32_32x32x16_bf16 v[48:63], v[156:159], v[222:225], v[48:63]
	ds_read_b64_tr_b16 v[222:223], v187 offset:0x3400
	ds_read_b64_tr_b16 v[224:225], v187 offset:0x3c00
	s_waitcnt lgkmcnt(0)
	v_mfma_f32_32x32x16_bf16 v[32:47], v[146:149], v[204:207], v[32:47]
	ds_read_b64_tr_b16 v[204:205], v187 offset:0x600
	ds_read_b64_tr_b16 v[206:207], v187 offset:0xe00
	v_mfma_f32_32x32x16_bf16 v[32:47], v[200:203], v[208:211], v[32:47]
	ds_read_b64_tr_b16 v[208:209], v187 offset:0x1600
	ds_read_b64_tr_b16 v[210:211], v187 offset:0x1e00
	v_mfma_f32_32x32x16_bf16 v[32:47], v[152:155], v[212:215], v[32:47]
	ds_read_b64_tr_b16 v[212:213], v187 offset:0x2600
	ds_read_b64_tr_b16 v[214:215], v187 offset:0x2e00
	v_mfma_f32_32x32x16_bf16 v[32:47], v[156:159], v[222:225], v[32:47]
	ds_read_b64_tr_b16 v[222:223], v187 offset:0x3600
	ds_read_b64_tr_b16 v[224:225], v187 offset:0x3e00
	s_waitcnt lgkmcnt(0)
	v_mfma_f32_32x32x16_bf16 v[16:31], v[146:149], v[204:207], v[16:31]
	v_max_f32_e32 v146, v81, v81
	v_max_f32_e32 v147, v80, v80
	v_max_f32_e32 v146, v147, v146
	v_max3_f32 v146, v146, v82, v83
	v_max3_f32 v146, v146, v84, v85
	v_max3_f32 v146, v146, v86, v87
	v_max3_f32 v146, v146, v88, v89
	v_max3_f32 v146, v146, v90, v91
	v_max3_f32 v146, v146, v92, v93
	v_mfma_f32_32x32x16_bf16 v[16:31], v[200:203], v[208:211], v[16:31]
	v_max3_f32 v146, v146, v94, v95
	v_max3_f32 v146, v146, v64, v65
	v_max3_f32 v146, v146, v66, v67
	v_max3_f32 v146, v146, v68, v69
	v_max3_f32 v146, v146, v70, v71
	v_max3_f32 v146, v146, v72, v73
	v_max3_f32 v146, v146, v74, v75
	v_max3_f32 v146, v146, v76, v77
	v_mfma_f32_32x32x16_bf16 v[16:31], v[152:155], v[212:215], v[16:31]
	v_max3_f32 v146, v146, v78, v79
	v_mov_b32_e32 v147, v146
	s_nop 1
	v_permlane32_swap_b32_e32 v146, v147
	v_max_f32_e32 v147, v147, v147
	v_max_f32_e32 v146, v146, v146
	v_max_f32_e32 v146, v146, v147
	v_sub_f32_e32 v147, v146, v150
	v_cmp_ge_f32_e32 vcc, s87, v147
	v_max_f32_e32 v147, v150, v150
	v_max_f32_e32 v146, v147, v146
	v_mfma_f32_32x32x16_bf16 v[16:31], v[156:159], v[222:225], v[16:31]
	v_sub_f32_e32 v147, v150, v146
	v_mul_f32_e32 v147, 0x3e0293ee, v147
	v_exp_f32_e32 v147, v147
	s_cmp_eq_u64 vcc, exec
	s_cselect_b64 s[42:43], -1, 0
	v_cndmask_b32_e64 v200, v147, 1.0, s[42:43]
	v_cmp_gt_f32_e32 vcc, 1.0, v200
	s_waitcnt vmcnt(0)
	s_barrier
	s_cbranch_vccz .LBB0_458
	s_and_saveexec_b64 s[6:7], s[40:41]
	ds_write_b32 v184, v200 offset:128
	s_or_b64 exec, exec, s[6:7]
	s_waitcnt lgkmcnt(0)
	v_add_u32_e32 v147, v183, v96
	ds_read_b128 v[152:155], v147 offset:224
	ds_read_b128 v[156:159], v147 offset:192
	ds_read_b128 v[202:205], v147 offset:160
	ds_read_b128 v[206:209], v147 offset:128
	s_waitcnt lgkmcnt(3)
	v_pk_mul_f32 v[12:13], v[12:13], v[152:153]
	s_waitcnt lgkmcnt(2)
	v_pk_mul_f32 v[8:9], v[8:9], v[156:157]
	s_waitcnt lgkmcnt(1)
	v_pk_mul_f32 v[4:5], v[4:5], v[202:203]
	v_pk_mul_f32 v[14:15], v[14:15], v[154:155]
	v_pk_mul_f32 v[10:11], v[10:11], v[158:159]
	v_pk_mul_f32 v[6:7], v[6:7], v[204:205]
	s_waitcnt lgkmcnt(0)
	v_pk_mul_f32 v[2:3], v[2:3], v[208:209]
	v_pk_mul_f32 v[0:1], v[0:1], v[206:207]
	v_pk_mul_f32 v[60:61], v[60:61], v[152:153]
	v_pk_mul_f32 v[56:57], v[56:57], v[156:157]
	v_pk_mul_f32 v[52:53], v[52:53], v[202:203]
	v_pk_mul_f32 v[62:63], v[62:63], v[154:155]
	v_pk_mul_f32 v[58:59], v[58:59], v[158:159]
	v_pk_mul_f32 v[54:55], v[54:55], v[204:205]
	v_pk_mul_f32 v[50:51], v[50:51], v[208:209]
	v_pk_mul_f32 v[48:49], v[48:49], v[206:207]
	v_pk_mul_f32 v[44:45], v[44:45], v[152:153]
	v_pk_mul_f32 v[40:41], v[40:41], v[156:157]
	v_pk_mul_f32 v[36:37], v[36:37], v[202:203]
	v_pk_mul_f32 v[46:47], v[46:47], v[154:155]
	v_pk_mul_f32 v[42:43], v[42:43], v[158:159]
	v_pk_mul_f32 v[38:39], v[38:39], v[204:205]
	v_pk_mul_f32 v[34:35], v[34:35], v[208:209]
	v_pk_mul_f32 v[32:33], v[32:33], v[206:207]
	v_pk_mul_f32 v[28:29], v[28:29], v[152:153]
	v_pk_mul_f32 v[24:25], v[24:25], v[156:157]
	v_pk_mul_f32 v[20:21], v[20:21], v[202:203]
	v_pk_mul_f32 v[30:31], v[30:31], v[154:155]
	v_pk_mul_f32 v[26:27], v[26:27], v[158:159]
	v_pk_mul_f32 v[22:23], v[22:23], v[204:205]
	v_pk_mul_f32 v[18:19], v[18:19], v[208:209]
	v_pk_mul_f32 v[16:17], v[16:17], v[206:207]

; __device__ __forceinline__ void partialSM(f32x16& p0, f32x16& p1, float& m_reg, float& mn, float& alpha) {
;   constexpr float C = SCALE * 1.4426950408889634f;
;   float pmax = p0[0]; for (int r = 1; r < 16; ++r) pmax = fmaxf(pmax, p0[r]); for (int r = 0; r < 16; ++r) pmax = fmaxf(pmax, p1[r]);
;   { auto rr = __builtin_amdgcn_permlane32_swap(__float_as_uint(pmax), __float_as_uint(pmax), false, false);
;     pmax = fmaxf(__uint_as_float(rr[0]), __uint_as_float(rr[1])); }
;   if (__builtin_expect(__all(pmax - m_reg <= THR / SCALE), 1)) { mn = m_reg; alpha = 1.f; }
;   else { mn = fmaxf(m_reg, pmax); alpha = __builtin_amdgcn_exp2f((m_reg - mn) * C); m_reg = mn; }
;   float mnC = -mn * C;
;   for (int r = 0; r < 16; ++r) p0[r] = fmaf(p0[r], C, mnC); for (int r = 0; r < 16; ++r) p1[r] = fmaf(p1[r], C, mnC);
;   for (int r = 0; r < 16; ++r) p0[r] = __builtin_amdgcn_exp2f(p0[r]);
; }
; __device__ __forceinline__ void finishSM(f32x16& p0, f32x16& p1, float alpha, float& l_reg, bf16x8& pa0, bf16x8& pa1, bf16x8& pa2, bf16x8& pa3) {
;   for (int r = 0; r < 16; ++r) p1[r] = __builtin_amdgcn_exp2f(p1[r]);
;   float ps = 0; for (int r = 0; r < 16; ++r) ps += p0[r]; for (int r = 0; r < 16; ++r) ps += p1[r];
;   { auto rr = __builtin_amdgcn_permlane32_swap(__float_as_uint(ps), __float_as_uint(ps), false, false);
;     ps = __uint_as_float(rr[0]) + __uint_as_float(rr[1]); }
;   l_reg = l_reg * alpha + ps;
;     ...
;   PK4(p0, 0, pa0); PK4(p0, 8, pa1); PK4(p1, 0, pa2); PK4(p1, 8, pa3);
;     ...
; }
; template <bool HALF> __device__ __forceinline__ void qkt(f32x16& p0, f32x16& p1, const char* Ks, const bf16x8* qr, int r32, int hi, int koff) {
;   p0 = f32x16{}; p1 = f32x16{};
;   for (int d0 = 0; d0 < (HALF ? 4 : 8); ++d0) { int cb = (d0 * 16 + hi * 8) * 2 + koff;
;     bf16x8 b0 = *reinterpret_cast<const bf16x8*>(Ks + KSWZ(r32, cb));
;     bf16x8 b1 = *reinterpret_cast<const bf16x8*>(Ks + KSWZ(32 + r32, cb));
;     p0 = __builtin_amdgcn_mfma_f32_32x32x16_bf16(b0, qr[d0], p0, 0, 0, 0);
;     p1 = __builtin_amdgcn_mfma_f32_32x32x16_bf16(b1, qr[d0], p1, 0, 0, 0); }
; }
; __device__ __forceinline__ int v_st(int k, int c) { const int kk = (k & ~0xC) | ((k & 4) << 1) | ((k & 8) >> 1); return ((kk >> 3) * 4 + (c >> 5)) * 512 + ((kk & 7) * 32 + (c & 31)) * 2; }
.LBB0_460:
	ds_read_b64_tr_b16 v[170:171], v186 offset:0
	ds_read_b64_tr_b16 v[172:173], v186 offset:0x800
	ds_read_b64_tr_b16 v[174:175], v186 offset:0x1000
	ds_read_b64_tr_b16 v[176:177], v186 offset:0x1800
	ds_read_b64_tr_b16 v[204:205], v186 offset:0x2000
	ds_read_b64_tr_b16 v[206:207], v186 offset:0x2800
	ds_read_b64_tr_b16 v[208:209], v186 offset:0x3000
	ds_read_b64_tr_b16 v[210:211], v186 offset:0x3800
	s_waitcnt lgkmcnt(0)
	s_nop 0
	v_mfma_f32_32x32x16_bf16 v[0:15], v[146:149], v[170:173], v[0:15]
	ds_read_b64_tr_b16 v[170:171], v186 offset:0x200
	ds_read_b64_tr_b16 v[172:173], v186 offset:0xa00
	v_mfma_f32_32x32x16_bf16 v[0:15], v[150:153], v[174:177], v[0:15]
	ds_read_b64_tr_b16 v[174:175], v186 offset:0x1200
	ds_read_b64_tr_b16 v[176:177], v186 offset:0x1a00
	v_mfma_f32_32x32x16_bf16 v[0:15], v[154:157], v[204:207], v[0:15]
	ds_read_b64_tr_b16 v[204:205], v186 offset:0x2200
	ds_read_b64_tr_b16 v[206:207], v186 offset:0x2a00
	v_mfma_f32_32x32x16_bf16 v[0:15], v[158:161], v[208:211], v[0:15]
	ds_read_b64_tr_b16 v[208:209], v186 offset:0x3200
	ds_read_b64_tr_b16 v[210:211], v186 offset:0x3a00
	s_waitcnt lgkmcnt(0)
	v_mfma_f32_32x32x16_bf16 v[48:63], v[146:149], v[170:173], v[48:63]
	ds_read_b64_tr_b16 v[170:171], v186 offset:0x400
	ds_read_b64_tr_b16 v[172:173], v186 offset:0xc00
	v_mfma_f32_32x32x16_bf16 v[48:63], v[150:153], v[174:177], v[48:63]
	ds_read_b64_tr_b16 v[174:175], v186 offset:0x1400
	ds_read_b64_tr_b16 v[176:177], v186 offset:0x1c00
	v_mfma_f32_32x32x16_bf16 v[48:63], v[154:157], v[204:207], v[48:63]
	ds_read_b64_tr_b16 v[204:205], v186 offset:0x2400
	ds_read_b64_tr_b16 v[206:207], v186 offset:0x2c00
	v_mfma_f32_32x32x16_bf16 v[48:63], v[158:161], v[208:211], v[48:63]
	ds_read_b64_tr_b16 v[208:209], v186 offset:0x3400
	ds_read_b64_tr_b16 v[210:211], v186 offset:0x3c00
	s_waitcnt lgkmcnt(0)
	v_mfma_f32_32x32x16_bf16 v[32:47], v[146:149], v[170:173], v[32:47]
	ds_read_b64_tr_b16 v[170:171], v186 offset:0x600
	ds_read_b64_tr_b16 v[172:173], v186 offset:0xe00
	v_mfma_f32_32x32x16_bf16 v[32:47], v[150:153], v[174:177], v[32:47]
	ds_read_b64_tr_b16 v[174:175], v186 offset:0x1600
	ds_read_b64_tr_b16 v[176:177], v186 offset:0x1e00
	v_mfma_f32_32x32x16_bf16 v[32:47], v[154:157], v[204:207], v[32:47]
	ds_read_b64_tr_b16 v[204:205], v186 offset:0x2600
	ds_read_b64_tr_b16 v[206:207], v186 offset:0x2e00
	v_mfma_f32_32x32x16_bf16 v[32:47], v[158:161], v[208:211], v[32:47]
	ds_read_b64_tr_b16 v[208:209], v186 offset:0x3600
	ds_read_b64_tr_b16 v[210:211], v186 offset:0x3e00
	s_waitcnt lgkmcnt(0)
	v_mfma_f32_32x32x16_bf16 v[16:31], v[146:149], v[170:173], v[16:31]
	v_max_f32_e32 v146, v81, v81
	v_max_f32_e32 v147, v80, v80
	v_max_f32_e32 v146, v147, v146
	v_max3_f32 v146, v146, v82, v83
	v_max3_f32 v146, v146, v84, v85
	v_max3_f32 v146, v146, v86, v87
	v_max3_f32 v146, v146, v88, v89
	v_max3_f32 v146, v146, v90, v91
	v_max3_f32 v146, v146, v92, v93
	v_mfma_f32_32x32x16_bf16 v[16:31], v[150:153], v[174:177], v[16:31]
	v_max3_f32 v146, v146, v94, v95
	v_max3_f32 v146, v146, v64, v65
	v_max3_f32 v146, v146, v66, v67
	v_max3_f32 v146, v146, v68, v69
	v_max3_f32 v146, v146, v70, v71
	v_max3_f32 v146, v146, v72, v73
	v_max3_f32 v146, v146, v74, v75
	v_max3_f32 v146, v146, v76, v77
	v_mfma_f32_32x32x16_bf16 v[16:31], v[154:157], v[204:207], v[16:31]
	v_max3_f32 v146, v146, v78, v79
	v_mov_b32_e32 v147, v146
	s_nop 1
	v_permlane32_swap_b32_e32 v146, v147
	v_max_f32_e32 v147, v147, v147
	v_max_f32_e32 v146, v146, v146
	v_max_f32_e32 v146, v146, v147
	v_sub_f32_e32 v147, v146, v201
	v_cmp_ge_f32_e32 vcc, s87, v147
	v_max_f32_e32 v147, v201, v201
	v_max_f32_e32 v147, v147, v146
	v_mfma_f32_32x32x16_bf16 v[16:31], v[158:161], v[208:211], v[16:31]
	v_sub_f32_e32 v146, v201, v147
	v_mul_f32_e32 v146, 0x3e0293ee, v146
	v_exp_f32_e32 v146, v146
	s_cmp_eq_u64 vcc, exec
	s_cselect_b64 s[42:43], -1, 0
	v_cndmask_b32_e64 v146, v146, 1.0, s[42:43]
	v_cmp_gt_f32_e32 vcc, 1.0, v146
	s_waitcnt vmcnt(0)
	s_barrier
	s_mov_b32 s54, 1
	s_cbranch_vccz .LBB0_464
	s_and_saveexec_b64 s[6:7], s[40:41]
	ds_write_b32 v184, v146 offset:128
	s_or_b64 exec, exec, s[6:7]
	s_waitcnt lgkmcnt(0)
	v_add_u32_e32 v142, v183, v96
	ds_read_b128 v[130:133], v142 offset:224
	ds_read_b128 v[134:137], v142 offset:192
	ds_read_b128 v[138:141], v142 offset:160
	ds_read_b128 v[142:145], v142 offset:128
	s_waitcnt lgkmcnt(3)
	v_pk_mul_f32 v[12:13], v[12:13], v[130:131]
	s_waitcnt lgkmcnt(2)
	v_pk_mul_f32 v[8:9], v[8:9], v[134:135]
	s_waitcnt lgkmcnt(1)
	v_pk_mul_f32 v[4:5], v[4:5], v[138:139]
	v_pk_mul_f32 v[14:15], v[14:15], v[132:133]
	v_pk_mul_f32 v[10:11], v[10:11], v[136:137]
	v_pk_mul_f32 v[6:7], v[6:7], v[140:141]
	s_waitcnt lgkmcnt(0)
	v_pk_mul_f32 v[2:3], v[2:3], v[144:145]
	v_pk_mul_f32 v[0:1], v[0:1], v[142:143]
	v_pk_mul_f32 v[60:61], v[60:61], v[130:131]
	v_pk_mul_f32 v[56:57], v[56:57], v[134:135]
	v_pk_mul_f32 v[52:53], v[52:53], v[138:139]
	v_pk_mul_f32 v[62:63], v[62:63], v[132:133]
	v_pk_mul_f32 v[58:59], v[58:59], v[136:137]
	v_pk_mul_f32 v[54:55], v[54:55], v[140:141]
	v_pk_mul_f32 v[50:51], v[50:51], v[144:145]
	v_pk_mul_f32 v[48:49], v[48:49], v[142:143]
	v_pk_mul_f32 v[44:45], v[44:45], v[130:131]
	v_pk_mul_f32 v[40:41], v[40:41], v[134:135]
	v_pk_mul_f32 v[36:37], v[36:37], v[138:139]
	v_pk_mul_f32 v[46:47], v[46:47], v[132:133]
	v_pk_mul_f32 v[42:43], v[42:43], v[136:137]
	v_pk_mul_f32 v[38:39], v[38:39], v[140:141]
	v_pk_mul_f32 v[34:35], v[34:35], v[144:145]
	v_pk_mul_f32 v[32:33], v[32:33], v[142:143]
	v_pk_mul_f32 v[28:29], v[28:29], v[130:131]
	v_pk_mul_f32 v[24:25], v[24:25], v[134:135]
	v_pk_mul_f32 v[20:21], v[20:21], v[138:139]
	v_pk_mul_f32 v[30:31], v[30:31], v[132:133]
	v_pk_mul_f32 v[26:27], v[26:27], v[136:137]
	v_pk_mul_f32 v[22:23], v[22:23], v[140:141]
	v_pk_mul_f32 v[18:19], v[18:19], v[144:145]
	v_pk_mul_f32 v[16:17], v[16:17], v[142:143]

; __device__ __forceinline__ unsigned hg_pk(float lo, float hi) { unsigned r; asm volatile("v_cvt_pk_bf16_f32 %0, %1, %2" : "=v"(r) : "v"(lo), "v"(hi)); return r; }
; #define HG_SB() __builtin_amdgcn_sched_barrier(0)
; __device__ __forceinline__ void ph_hgrn_out2(const P& p, int l, int jmin, int gw, int nw, int lane) {
;     ...
;       const bool hasref = dir == 0 ? (I > 0) : (I < 3); const int refrow = hasref ? (dir == 0 ? rbase + 16 * I - 1 : rbase + 16 * (I + 1)) : rowi;
;       const bf16_t* sb = WSP(bf16_t, WS_SB) + ((size_t)(c * 8 + hd) * 128 + r16) * 128 + 8 * q;
;       f32x4 rv[4][2], bv[4][2]; u32x4 qw[4]; hg_bf16x8 sv[16];
; #pragma unroll
;       for (int ks = 0; ks < 4; ++ks) { rv[ks][0] = *(const f32x4*)(BC + (size_t)refrow * 1024 + colb + 32 * ks); rv[ks][1] = *(const f32x4*)(BC + (size_t)refrow * 1024 + colb + 32 * ks + 4);
;         bv[ks][0] = *(const f32x4*)(BC + (size_t)rowi * 1024 + colb + 32 * ks); bv[ks][1] = *(const f32x4*)(BC + (size_t)rowi * 1024 + colb + 32 * ks + 4);
;         qw[ks] = *(const u32x4*)(proj + (size_t)rowi * INW + C_HQ + colb + 32 * ks); }
; #pragma unroll
;       for (int u = 0; u < 16; ++u) sv[u] = *(const hg_bf16x8*)(sb + (size_t)(16 * (u >> 2)) * 128 + 32 * (u & 3));
;       HG_SB();
;       float refv[4][8]; hg_bf16x8 Qs[4], Qe[4];
; #pragma unroll
;       for (int ks = 0; ks < 4; ++ks) {
; #pragma unroll
;         for (int jj = 0; jj < 4; ++jj) { refv[ks][jj] = hasref ? rv[ks][0][jj] : 0.f; refv[ks][4 + jj] = hasref ? rv[ks][1][jj] : 0.f; }
;         u32x4 sw, ew;
; #pragma unroll
;         for (int jj = 0; jj < 4; ++jj) { const float qa = __uint_as_float(qw[ks][jj] << 16), qb = __uint_as_float(qw[ks][jj] & 0xffff0000u);
;           const float ba = jj < 2 ? bv[ks][0][2 * jj] : bv[ks][1][2 * jj - 4], bb = jj < 2 ? bv[ks][0][2 * jj + 1] : bv[ks][1][2 * jj - 3];
;           sw[jj] = hg_pk(qa * __expf(ba - refv[ks][2 * jj]), qb * __expf(bb - refv[ks][2 * jj + 1])); ew[jj] = hg_pk(qa * __expf(ba), qb * __expf(bb)); }
;         Qs[ks] = __builtin_bit_cast(hg_bf16x8, sw); Qe[ks] = __builtin_bit_cast(hg_bf16x8, ew); }
.LBB0_533:
	s_lshl_b32 s56, s6, 2
	s_and_b64 s[30:31], s[14:15], exec
	v_lshl_add_u32 v48, s6, 9, v95
	s_cselect_b32 s6, 0, 3
	s_cselect_b32 s30, s24, s93
	s_cmp_eq_u32 s64, s6
	s_cselect_b64 vcc, -1, 0
	s_and_b64 s[6:7], s[14:15], exec
	s_cselect_b32 s6, s96, s3
	v_mov_b32_e32 v49, s6
	v_cndmask_b32_e32 v50, v49, v188, vcc
	v_ashrrev_i32_e32 v51, 31, v50
	v_lshlrev_b64 v[50:51], 12, v[50:51]
	v_ashrrev_i32_e32 v49, 31, v48
	v_lshl_add_u64 v[50:51], s[20:21], 0, v[50:51]
	v_lshlrev_b64 v[202:203], 2, v[48:49]
	v_lshl_add_u64 v[52:53], v[50:51], 0, v[202:203]
	v_lshlrev_b64 v[204:205], 1, v[48:49]
	v_lshl_add_u64 v[66:67], v[190:191], 0, v[202:203]
	v_lshl_add_u64 v[68:69], v[192:193], 0, v[204:205]
	global_load_dwordx4 v[48:51], v[52:53], off offset:16
	global_load_dwordx4 v[110:113], v[52:53], off
	global_load_dwordx4 v[154:157], v[66:67], off offset:16
	global_load_dwordx4 v[212:215], v[66:67], off
	global_load_dwordx4 v[232:235], v[52:53], off offset:144
	global_load_dwordx4 v[236:239], v[52:53], off offset:128
	global_load_dwordx4 v[54:57], v[66:67], off offset:144
	global_load_dwordx4 v[240:243], v[66:67], off offset:128
	global_load_dwordx4 v[224:227], v[68:69], off
	global_load_dwordx4 v[244:247], v[68:69], off offset:64
	global_load_dwordx4 v[166:169], v[52:53], off offset:272
	global_load_dwordx4 v[170:173], v[52:53], off offset:256
	global_load_dwordx4 v[58:61], v[66:67], off offset:272
	global_load_dwordx4 v[162:165], v[66:67], off offset:256
	global_load_dwordx4 v[146:149], v[52:53], off offset:400
	global_load_dwordx4 v[150:153], v[52:53], off offset:384
	global_load_dwordx4 v[62:65], v[66:67], off offset:400
	global_load_dwordx4 v[142:145], v[66:67], off offset:384
	global_load_dwordx4 v[158:161], v[68:69], off offset:128
	global_load_dwordx4 v[134:137], v[68:69], off offset:192
	s_lshl_b32 s6, s30, 3
	s_or_b32 s6, s6, s56
	s_or_b32 s6, s6, s67
	s_ashr_i32 s7, s6, 31
	s_lshl_b64 s[6:7], s[6:7], 15
	v_lshl_add_u64 v[206:207], v[182:183], 0, s[6:7]
	v_add_co_u32_e64 v52, s[56:57], s25, v206
	s_movk_i32 s6, 0x2000
	s_nop 0
	v_addc_co_u32_e64 v53, s[56:57], 0, v207, s[56:57]
	v_add_co_u32_e64 v114, s[56:57], s6, v206
	s_movk_i32 s6, 0x4000
	s_nop 0
	v_addc_co_u32_e64 v115, s[56:57], 0, v207, s[56:57]
	v_add_co_u32_e64 v130, s[56:57], s11, v206
	global_load_dwordx4 v[78:81], v[206:207], off
	global_load_dwordx4 v[74:77], v[206:207], off offset:64
	global_load_dwordx4 v[70:73], v[206:207], off offset:128
	global_load_dwordx4 v[66:69], v[206:207], off offset:192
	v_addc_co_u32_e64 v131, s[56:57], 0, v207, s[56:57]
	v_add_co_u32_e64 v208, s[56:57], s6, v206
	global_load_dwordx4 v[82:85], v[52:53], off offset:64
	global_load_dwordx4 v[86:89], v[52:53], off offset:128
	global_load_dwordx4 v[106:109], v[114:115], off offset:-4096
	global_load_dwordx4 v[90:93], v[114:115], off
	global_load_dwordx4 v[98:101], v[114:115], off offset:64
	global_load_dwordx4 v[102:105], v[114:115], off offset:128
	v_addc_co_u32_e64 v209, s[56:57], 0, v207, s[56:57]
	global_load_dwordx4 v[114:117], v[114:115], off offset:192
	s_nop 0
	global_load_dwordx4 v[118:121], v[208:209], off offset:-4096
	global_load_dwordx4 v[138:141], v[52:53], off offset:192
	global_load_dwordx4 v[122:125], v[130:131], off offset:64
	global_load_dwordx4 v[126:129], v[130:131], off offset:128
	s_nop 0
	global_load_dwordx4 v[130:133], v[130:131], off offset:192
	s_waitcnt vmcnt(16)
	v_cndmask_b32_e64 v222, v110, 0, vcc
	v_cndmask_b32_e64 v221, v111, 0, vcc
	v_cndmask_b32_e64 v189, v48, 0, vcc
	v_sub_f32_e32 v48, v212, v222
	v_cndmask_b32_e64 v175, v51, 0, vcc
	v_sub_f32_e32 v51, v213, v221
	v_mul_f32_e32 v48, 0x3fb8aa3b, v48
	v_mul_f32_e32 v51, 0x3fb8aa3b, v51
	v_exp_f32_e32 v48, v48
	v_exp_f32_e32 v51, v51
	v_cndmask_b32_e64 v177, v49, 0, vcc
	v_cndmask_b32_e64 v96, v50, 0, vcc
	v_lshlrev_b32_e32 v49, 16, v224
	v_and_b32_e32 v50, 0xffff0000, v224
	v_cndmask_b32_e64 v211, v112, 0, vcc
	v_mul_f32_e32 v48, v48, v49
	v_mul_f32_e32 v53, 0x3fb8aa3b, v213
	v_mul_f32_e32 v51, v51, v50
	v_mul_f32_e32 v52, 0x3fb8aa3b, v212
	v_exp_f32_e32 v53, v53
	v_cvt_pk_bf16_f32 v48, v48, v51
	v_sub_f32_e32 v51, v214, v211
	v_exp_f32_e32 v52, v52
	v_mul_f32_e32 v51, 0x3fb8aa3b, v51
	v_exp_f32_e32 v51, v51
	v_mul_f32_e32 v50, v53, v50
	v_cndmask_b32_e64 v210, v113, 0, vcc
	v_mul_f32_e32 v49, v52, v49
	v_cvt_pk_bf16_f32 v110, v49, v50
	v_lshlrev_b32_e32 v50, 16, v225
	v_mul_f32_e32 v49, v51, v50
	v_sub_f32_e32 v51, v215, v210
	v_mul_f32_e32 v51, 0x3fb8aa3b, v51
	v_exp_f32_e32 v51, v51
	v_mul_f32_e32 v111, 0x3fb8aa3b, v215
	v_exp_f32_e32 v111, v111
	v_and_b32_e32 v52, 0xffff0000, v225
	v_mul_f32_e32 v51, v51, v52
	v_mul_f32_e32 v53, 0x3fb8aa3b, v214
	v_cvt_pk_bf16_f32 v49, v49, v51
	v_mul_f32_e32 v51, v111, v52
	v_sub_f32_e32 v52, v154, v189
	v_exp_f32_e32 v53, v53
	v_mul_f32_e32 v52, 0x3fb8aa3b, v52
	v_exp_f32_e32 v52, v52
	v_mul_f32_e32 v113, 0x3fb8aa3b, v155
	v_mul_f32_e32 v50, v53, v50
	v_cvt_pk_bf16_f32 v111, v50, v51
	v_lshlrev_b32_e32 v51, 16, v226
	v_mul_f32_e32 v50, v52, v51
	v_sub_f32_e32 v52, v155, v177
	v_mul_f32_e32 v52, 0x3fb8aa3b, v52
	v_exp_f32_e32 v52, v52
	v_exp_f32_e32 v113, v113
	v_and_b32_e32 v53, 0xffff0000, v226
	v_mul_f32_e32 v112, 0x3fb8aa3b, v154
	v_mul_f32_e32 v52, v52, v53
	v_cvt_pk_bf16_f32 v50, v50, v52
	v_mul_f32_e32 v52, v113, v53
	v_sub_f32_e32 v53, v156, v96
	v_exp_f32_e32 v112, v112
	v_mul_f32_e32 v53, 0x3fb8aa3b, v53
	v_exp_f32_e32 v53, v53
	v_mul_f32_e32 v154, 0x3fb8aa3b, v156
	v_mul_f32_e32 v51, v112, v51
	v_cvt_pk_bf16_f32 v112, v51, v52
	v_lshlrev_b32_e32 v52, 16, v227
	v_mul_f32_e32 v51, v53, v52
	v_sub_f32_e32 v53, v157, v175
	v_mul_f32_e32 v53, 0x3fb8aa3b, v53
; __device__ __forceinline__ unsigned hg_pk(float lo, float hi) { unsigned r; asm volatile("v_cvt_pk_bf16_f32 %0, %1, %2" : "=v"(r) : "v"(lo), "v"(hi)); return r; }
; __device__ __forceinline__ void ph_hgrn_out2(const P& p, int l, int jmin, int gw, int nw, int lane) {
;     ...
;       float refv[4][8]; hg_bf16x8 Qs[4], Qe[4];
; #pragma unroll
;       for (int ks = 0; ks < 4; ++ks) {
; #pragma unroll
;         for (int jj = 0; jj < 4; ++jj) { refv[ks][jj] = hasref ? rv[ks][0][jj] : 0.f; refv[ks][4 + jj] = hasref ? rv[ks][1][jj] : 0.f; }
;         u32x4 sw, ew;
; #pragma unroll
;         for (int jj = 0; jj < 4; ++jj) { const float qa = __uint_as_float(qw[ks][jj] << 16), qb = __uint_as_float(qw[ks][jj] & 0xffff0000u);
;           const float ba = jj < 2 ? bv[ks][0][2 * jj] : bv[ks][1][2 * jj - 4], bb = jj < 2 ? bv[ks][0][2 * jj + 1] : bv[ks][1][2 * jj - 3];
;           sw[jj] = hg_pk(qa * __expf(ba - refv[ks][2 * jj]), qb * __expf(bb - refv[ks][2 * jj + 1])); ew[jj] = hg_pk(qa * __expf(ba), qb * __expf(bb)); }
;         Qs[ks] = __builtin_bit_cast(hg_bf16x8, sw); Qe[ks] = __builtin_bit_cast(hg_bf16x8, ew); }
	v_exp_f32_e32 v53, v53
	v_exp_f32_e32 v154, v154
	v_mul_f32_e32 v155, 0x3fb8aa3b, v157
	v_exp_f32_e32 v155, v155
	v_and_b32_e32 v113, 0xffff0000, v227
	v_mul_f32_e32 v53, v53, v113
	v_mul_f32_e32 v52, v154, v52
	v_cndmask_b32_e64 v230, v236, 0, vcc
	v_cndmask_b32_e64 v229, v237, 0, vcc
	v_cvt_pk_bf16_f32 v51, v51, v53
	v_mul_f32_e32 v53, v155, v113
	v_cvt_pk_bf16_f32 v113, v52, v53
	v_sub_f32_e32 v52, v240, v230
	v_sub_f32_e32 v155, v241, v229
	v_mul_f32_e32 v52, 0x3fb8aa3b, v52
	v_mul_f32_e32 v155, 0x3fb8aa3b, v155
	v_exp_f32_e32 v52, v52
	v_exp_f32_e32 v155, v155
	v_lshlrev_b32_e32 v53, 16, v244
	v_and_b32_e32 v154, 0xffff0000, v244
	v_cndmask_b32_e64 v228, v238, 0, vcc
	v_mul_f32_e32 v52, v52, v53
	v_mul_f32_e32 v155, v155, v154
	v_mul_f32_e32 v156, 0x3fb8aa3b, v240
	v_mul_f32_e32 v157, 0x3fb8aa3b, v241
	v_cvt_pk_bf16_f32 v52, v52, v155
	v_sub_f32_e32 v155, v242, v228
	v_exp_f32_e32 v156, v156
	v_exp_f32_e32 v157, v157
	v_mul_f32_e32 v155, 0x3fb8aa3b, v155
	v_exp_f32_e32 v155, v155
	v_cndmask_b32_e64 v227, v239, 0, vcc
	v_mul_f32_e32 v53, v156, v53
	v_mul_f32_e32 v154, v157, v154
	v_lshlrev_b32_e32 v156, 16, v245
	v_cvt_pk_bf16_f32 v154, v53, v154
	v_mul_f32_e32 v53, v155, v156
	v_sub_f32_e32 v155, v243, v227
	v_mul_f32_e32 v155, 0x3fb8aa3b, v155
	v_exp_f32_e32 v155, v155
	v_mul_f32_e32 v212, 0x3fb8aa3b, v242
	v_mul_f32_e32 v213, 0x3fb8aa3b, v243
	v_exp_f32_e32 v212, v212
	v_exp_f32_e32 v213, v213
	v_and_b32_e32 v157, 0xffff0000, v245
	v_cndmask_b32_e64 v226, v232, 0, vcc
	v_cndmask_b32_e64 v225, v233, 0, vcc
	v_mul_f32_e32 v155, v155, v157
	v_cvt_pk_bf16_f32 v53, v53, v155
	v_mul_f32_e32 v155, v212, v156
	v_mul_f32_e32 v156, v213, v157
	v_sub_f32_e32 v157, v54, v226
	v_sub_f32_e32 v213, v55, v225
	v_mul_f32_e32 v157, 0x3fb8aa3b, v157
	v_mul_f32_e32 v213, 0x3fb8aa3b, v213
	v_exp_f32_e32 v157, v157
	v_exp_f32_e32 v213, v213
	v_mul_f32_e32 v54, 0x3fb8aa3b, v54
	v_cvt_pk_bf16_f32 v155, v155, v156
	v_lshlrev_b32_e32 v156, 16, v246
	v_and_b32_e32 v212, 0xffff0000, v246
	v_exp_f32_e32 v214, v54
	v_mul_f32_e32 v54, 0x3fb8aa3b, v55
	v_cndmask_b32_e64 v223, v234, 0, vcc
	v_mul_f32_e32 v157, v157, v156
	v_exp_f32_e32 v55, v54
	v_mul_f32_e32 v54, v213, v212
	v_cvt_pk_bf16_f32 v54, v157, v54
	v_sub_f32_e32 v157, v56, v223
	v_mul_f32_e32 v157, 0x3fb8aa3b, v157
	v_exp_f32_e32 v157, v157
	v_cndmask_b32_e64 v224, v235, 0, vcc
	v_mul_f32_e32 v156, v214, v156
	v_mul_f32_e32 v55, v55, v212
	v_lshlrev_b32_e32 v212, 16, v247
	v_cvt_pk_bf16_f32 v156, v156, v55
	v_mul_f32_e32 v55, v157, v212
	v_sub_f32_e32 v157, v57, v224
	v_mul_f32_e32 v157, 0x3fb8aa3b, v157
	v_mul_f32_e32 v56, 0x3fb8aa3b, v56
	v_exp_f32_e32 v157, v157
	v_exp_f32_e32 v56, v56
	v_mul_f32_e32 v57, 0x3fb8aa3b, v57
	v_exp_f32_e32 v57, v57
	v_and_b32_e32 v213, 0xffff0000, v247
	v_mul_f32_e32 v157, v157, v213
	v_mul_f32_e32 v56, v56, v212
	v_cndmask_b32_e64 v233, v170, 0, vcc
	v_cvt_pk_bf16_f32 v55, v55, v157
	v_mul_f32_e32 v57, v57, v213
	v_cvt_pk_bf16_f32 v157, v56, v57
	v_sub_f32_e32 v56, v162, v233
	v_mul_f32_e32 v56, 0x3fb8aa3b, v56
	v_mul_f32_e32 v162, 0x3fb8aa3b, v162
	v_exp_f32_e32 v56, v56
	v_exp_f32_e32 v162, v162
	v_cndmask_b32_e64 v232, v171, 0, vcc
	v_cndmask_b32_e64 v170, v167, 0, vcc
	v_cndmask_b32_e64 v171, v172, 0, vcc
	v_cndmask_b32_e64 v167, v169, 0, vcc
	v_lshlrev_b32_e32 v57, 16, v158
	v_sub_f32_e32 v169, v163, v232
	v_mul_f32_e32 v56, v56, v57
	v_mul_f32_e32 v169, 0x3fb8aa3b, v169
	v_mul_f32_e32 v163, 0x3fb8aa3b, v163
	v_mul_f32_e32 v57, v162, v57
	v_sub_f32_e32 v162, v164, v171
	v_exp_f32_e32 v169, v169
	v_exp_f32_e32 v163, v163
	v_mul_f32_e32 v162, 0x3fb8aa3b, v162
	v_exp_f32_e32 v162, v162
	v_and_b32_e32 v158, 0xffff0000, v158
	v_cndmask_b32_e64 v231, v166, 0, vcc
	v_cndmask_b32_e64 v166, v168, 0, vcc
	v_cndmask_b32_e64 v168, v173, 0, vcc
	v_mul_f32_e32 v169, v169, v158
	v_mul_f32_e32 v158, v163, v158
	v_lshlrev_b32_e32 v163, 16, v159
	v_cvt_pk_bf16_f32 v56, v56, v169
	v_cvt_pk_bf16_f32 v158, v57, v158
	v_mul_f32_e32 v57, v162, v163
	v_sub_f32_e32 v162, v165, v168
	v_mul_f32_e32 v162, 0x3fb8aa3b, v162
	v_exp_f32_e32 v162, v162
	v_mul_f32_e32 v164, 0x3fb8aa3b, v164
	v_exp_f32_e32 v164, v164
	v_mul_f32_e32 v165, 0x3fb8aa3b, v165
	v_exp_f32_e32 v165, v165
	v_and_b32_e32 v159, 0xffff0000, v159
	v_mul_f32_e32 v162, v162, v159
	v_cvt_pk_bf16_f32 v57, v57, v162
	v_mul_f32_e32 v162, v164, v163
	v_sub_f32_e32 v163, v58, v231
	v_sub_f32_e32 v164, v59, v170
	v_mul_f32_e32 v58, 0x3fb8aa3b, v58
	v_mul_f32_e32 v159, v165, v159
	v_mul_f32_e32 v164, 0x3fb8aa3b, v164
	v_exp_f32_e32 v165, v58
	v_mul_f32_e32 v58, 0x3fb8aa3b, v59
	v_mul_f32_e32 v163, 0x3fb8aa3b, v163
	v_exp_f32_e32 v164, v164
	v_exp_f32_e32 v59, v58
	v_exp_f32_e32 v163, v163
	v_cvt_pk_bf16_f32 v159, v162, v159
	v_lshlrev_b32_e32 v162, 16, v160
	v_and_b32_e32 v160, 0xffff0000, v160
	v_mul_f32_e32 v58, v164, v160
	v_mul_f32_e32 v59, v59, v160
	v_sub_f32_e32 v160, v60, v166
	v_mul_f32_e32 v163, v163, v162
	v_mul_f32_e32 v160, 0x3fb8aa3b, v160
	v_cvt_pk_bf16_f32 v58, v163, v58
	v_exp_f32_e32 v163, v160
	v_mul_f32_e32 v162, v165, v162
	v_cvt_pk_bf16_f32 v160, v162, v59
	v_lshlrev_b32_e32 v162, 16, v161
	v_mul_f32_e32 v59, v163, v162
	v_sub_f32_e32 v163, v61, v167
	v_mul_f32_e32 v60, 0x3fb8aa3b, v60
	v_mul_f32_e32 v163, 0x3fb8aa3b, v163
	v_exp_f32_e32 v60, v60
	v_mul_f32_e32 v61, 0x3fb8aa3b, v61
	v_exp_f32_e32 v163, v163
	v_exp_f32_e32 v61, v61
	v_and_b32_e32 v161, 0xffff0000, v161
	v_mul_f32_e32 v60, v60, v162
	v_cndmask_b32_e64 v164, v150, 0, vcc
	v_mul_f32_e32 v163, v163, v161
	v_cvt_pk_bf16_f32 v59, v59, v163
	v_mul_f32_e32 v61, v61, v161
	v_cvt_pk_bf16_f32 v161, v60, v61
	v_sub_f32_e32 v60, v142, v164
	v_mul_f32_e32 v60, 0x3fb8aa3b, v60
; __device__ __forceinline__ unsigned hg_pk(float lo, float hi) { unsigned r; asm volatile("v_cvt_pk_bf16_f32 %0, %1, %2" : "=v"(r) : "v"(lo), "v"(hi)); return r; }
; #define HG_SB() __builtin_amdgcn_sched_barrier(0)
; __device__ __forceinline__ void ph_hgrn_out2(const P& p, int l, int jmin, int gw, int nw, int lane) {
;     ...
;         for (int jj = 0; jj < 4; ++jj) { const float qa = __uint_as_float(qw[ks][jj] << 16), qb = __uint_as_float(qw[ks][jj] & 0xffff0000u);
;           const float ba = jj < 2 ? bv[ks][0][2 * jj] : bv[ks][1][2 * jj - 4], bb = jj < 2 ? bv[ks][0][2 * jj + 1] : bv[ks][1][2 * jj - 3];
;           sw[jj] = hg_pk(qa * __expf(ba - refv[ks][2 * jj]), qb * __expf(bb - refv[ks][2 * jj + 1])); ew[jj] = hg_pk(qa * __expf(ba), qb * __expf(bb)); }
;         Qs[ks] = __builtin_bit_cast(hg_bf16x8, sw); Qe[ks] = __builtin_bit_cast(hg_bf16x8, ew); }
; #pragma unroll
;       for (int u = 0; u < 16; ++u) O[u >> 2] = __builtin_amdgcn_mfma_f32_16x16x32_bf16(Qe[u & 3], sv[u], O[u >> 2], 0, 0, 0);
;       HG_SB();
; #pragma unroll
;       for (int u = 0; u < 16; ++u) sv[u] = *(const hg_bf16x8*)(sb + (size_t)(16 * (4 + (u >> 2))) * 128 + 32 * (u & 3));
;       HG_SB();
; #pragma unroll
;       for (int u = 0; u < 16; ++u) O[4 + (u >> 2)] = __builtin_amdgcn_mfma_f32_16x16x32_bf16(Qe[u & 3], sv[u], O[4 + (u >> 2)], 0, 0, 0);
	v_mul_f32_e32 v142, 0x3fb8aa3b, v142
	v_exp_f32_e32 v60, v60
	v_exp_f32_e32 v142, v142
	v_cndmask_b32_e64 v163, v151, 0, vcc
	v_cndmask_b32_e64 v150, v147, 0, vcc
	v_cndmask_b32_e64 v151, v152, 0, vcc
	v_cndmask_b32_e64 v147, v149, 0, vcc
	v_lshlrev_b32_e32 v61, 16, v134
	v_sub_f32_e32 v149, v143, v163
	v_mul_f32_e32 v60, v60, v61
	v_mul_f32_e32 v149, 0x3fb8aa3b, v149
	v_mul_f32_e32 v143, 0x3fb8aa3b, v143
	v_mul_f32_e32 v61, v142, v61
	v_sub_f32_e32 v142, v144, v151
	v_exp_f32_e32 v149, v149
	v_exp_f32_e32 v143, v143
	v_mul_f32_e32 v142, 0x3fb8aa3b, v142
	v_exp_f32_e32 v142, v142
	v_and_b32_e32 v134, 0xffff0000, v134
	v_cndmask_b32_e64 v162, v146, 0, vcc
	v_cndmask_b32_e64 v146, v148, 0, vcc
	v_cndmask_b32_e64 v148, v153, 0, vcc
	v_mul_f32_e32 v149, v149, v134
	v_mul_f32_e32 v134, v143, v134
	v_lshlrev_b32_e32 v143, 16, v135
	v_cvt_pk_bf16_f32 v60, v60, v149
	v_cvt_pk_bf16_f32 v134, v61, v134
	v_mul_f32_e32 v61, v142, v143
	v_sub_f32_e32 v142, v145, v148
	v_mul_f32_e32 v142, 0x3fb8aa3b, v142
	v_exp_f32_e32 v142, v142
	v_mul_f32_e32 v144, 0x3fb8aa3b, v144
	v_exp_f32_e32 v144, v144
	v_mul_f32_e32 v145, 0x3fb8aa3b, v145
	v_exp_f32_e32 v145, v145
	v_and_b32_e32 v135, 0xffff0000, v135
	v_mul_f32_e32 v142, v142, v135
	v_cvt_pk_bf16_f32 v61, v61, v142
	v_mul_f32_e32 v142, v144, v143
	v_sub_f32_e32 v143, v62, v162
	v_sub_f32_e32 v144, v63, v150
	v_mul_f32_e32 v62, 0x3fb8aa3b, v62
	v_mul_f32_e32 v135, v145, v135
	v_mul_f32_e32 v144, 0x3fb8aa3b, v144
	v_exp_f32_e32 v145, v62
	v_mul_f32_e32 v62, 0x3fb8aa3b, v63
	v_mul_f32_e32 v143, 0x3fb8aa3b, v143
	v_exp_f32_e32 v144, v144
	v_exp_f32_e32 v63, v62
	s_waitcnt vmcnt(0)
	v_mfma_f32_16x16x32_bf16 v[0:3], v[110:113], v[78:81], v[0:3]
	v_exp_f32_e32 v143, v143
	v_cvt_pk_bf16_f32 v135, v142, v135
	v_lshlrev_b32_e32 v142, 16, v136
	v_mfma_f32_16x16x32_bf16 v[4:7], v[110:113], v[106:109], v[4:7]
	v_and_b32_e32 v136, 0xffff0000, v136
	v_mul_f32_e32 v62, v144, v136
	v_mul_f32_e32 v63, v63, v136
	v_mfma_f32_16x16x32_bf16 v[36:39], v[110:113], v[90:93], v[36:39]
	v_mul_f32_e32 v143, v143, v142
	v_cvt_pk_bf16_f32 v62, v143, v62
	v_mul_f32_e32 v142, v145, v142
	v_mfma_f32_16x16x32_bf16 v[32:35], v[110:113], v[118:121], v[32:35]
	v_cvt_pk_bf16_f32 v136, v142, v63
	v_sub_f32_e32 v63, v64, v146
	v_mul_f32_e32 v63, 0x3fb8aa3b, v63
	v_mfma_f32_16x16x32_bf16 v[0:3], v[154:157], v[74:77], v[0:3]
	v_sub_f32_e32 v143, v65, v147
	v_exp_f32_e32 v63, v63
	v_mul_f32_e32 v143, 0x3fb8aa3b, v143
	v_mfma_f32_16x16x32_bf16 v[4:7], v[154:157], v[82:85], v[4:7]
	v_mul_f32_e32 v64, 0x3fb8aa3b, v64
	v_mul_f32_e32 v65, 0x3fb8aa3b, v65
	v_exp_f32_e32 v143, v143
	v_mfma_f32_16x16x32_bf16 v[36:39], v[154:157], v[98:101], v[36:39]
	v_exp_f32_e32 v64, v64
	v_exp_f32_e32 v65, v65
	v_lshlrev_b32_e32 v142, 16, v137
	v_mfma_f32_16x16x32_bf16 v[32:35], v[154:157], v[122:125], v[32:35]
	v_and_b32_e32 v137, 0xffff0000, v137
	v_mul_f32_e32 v63, v63, v142
	v_mul_f32_e32 v78, v143, v137
	v_mfma_f32_16x16x32_bf16 v[0:3], v[158:161], v[70:73], v[0:3]
	v_cvt_pk_bf16_f32 v63, v63, v78
	v_mul_f32_e32 v64, v64, v142
	v_mul_f32_e32 v65, v65, v137
	v_mfma_f32_16x16x32_bf16 v[4:7], v[158:161], v[86:89], v[4:7]
	v_cvt_pk_bf16_f32 v137, v64, v65
	v_mfma_f32_16x16x32_bf16 v[36:39], v[158:161], v[102:105], v[36:39]
	v_mfma_f32_16x16x32_bf16 v[32:35], v[158:161], v[126:129], v[32:35]
	v_mfma_f32_16x16x32_bf16 v[0:3], v[134:137], v[66:69], v[0:3]
	v_mfma_f32_16x16x32_bf16 v[4:7], v[134:137], v[138:141], v[4:7]
	v_mfma_f32_16x16x32_bf16 v[36:39], v[134:137], v[114:117], v[36:39]
	v_mfma_f32_16x16x32_bf16 v[32:35], v[134:137], v[130:133], v[32:35]
	s_movk_i32 s6, 0x5000
	v_add_co_u32_e32 v92, vcc, s6, v206
	s_movk_i32 s6, 0x7000
	s_nop 0
	v_addc_co_u32_e32 v93, vcc, 0, v207, vcc
	v_add_co_u32_e32 v106, vcc, s82, v206
	global_load_dwordx4 v[64:67], v[208:209], off offset:64
	global_load_dwordx4 v[68:71], v[208:209], off offset:128
	v_addc_co_u32_e32 v107, vcc, 0, v207, vcc
	global_load_dwordx4 v[72:75], v[208:209], off offset:192
	global_load_dwordx4 v[76:79], v[106:107], off offset:-4096
	global_load_dwordx4 v[80:83], v[92:93], off offset:64
	global_load_dwordx4 v[84:87], v[92:93], off offset:128
	global_load_dwordx4 v[88:91], v[106:107], off
	global_load_dwordx4 v[98:101], v[106:107], off offset:64
	global_load_dwordx4 v[102:105], v[106:107], off offset:128
	s_nop 0
	global_load_dwordx4 v[106:109], v[106:107], off offset:192
	v_add_co_u32_e32 v138, vcc, s6, v206
	s_nop 1
	v_addc_co_u32_e32 v139, vcc, 0, v207, vcc
	global_load_dwordx4 v[114:117], v[92:93], off offset:192
	global_load_dwordx4 v[118:121], v[138:139], off
	global_load_dwordx4 v[122:125], v[138:139], off offset:64
	global_load_dwordx4 v[126:129], v[138:139], off offset:128
	global_load_dwordx4 v[130:133], v[208:209], off
	s_nop 0
	global_load_dwordx4 v[138:141], v[138:139], off offset:192
	s_waitcnt vmcnt(1)
	v_mfma_f32_16x16x32_bf16 v[28:31], v[110:113], v[130:133], v[28:31]
	s_or_b64 s[6:7], s[72:73], s[14:15]
	s_andn2_b64 vcc, exec, s[6:7]
	v_mfma_f32_16x16x32_bf16 v[24:27], v[110:113], v[76:79], v[24:27]
	v_mfma_f32_16x16x32_bf16 v[20:23], v[110:113], v[88:91], v[20:23]
	v_mfma_f32_16x16x32_bf16 v[8:11], v[110:113], v[118:121], v[8:11]
	v_mfma_f32_16x16x32_bf16 v[28:31], v[154:157], v[64:67], v[28:31]
	v_mfma_f32_16x16x32_bf16 v[24:27], v[154:157], v[80:83], v[24:27]
	v_mfma_f32_16x16x32_bf16 v[20:23], v[154:157], v[98:101], v[20:23]
	v_mfma_f32_16x16x32_bf16 v[8:11], v[154:157], v[122:125], v[8:11]
	v_mfma_f32_16x16x32_bf16 v[28:31], v[158:161], v[68:71], v[28:31]
	v_mfma_f32_16x16x32_bf16 v[24:27], v[158:161], v[84:87], v[24:27]
	v_mfma_f32_16x16x32_bf16 v[20:23], v[158:161], v[102:105], v[20:23]
	v_mfma_f32_16x16x32_bf16 v[8:11], v[158:161], v[126:129], v[8:11]
	v_mfma_f32_16x16x32_bf16 v[28:31], v[134:137], v[72:75], v[28:31]
	v_lshl_add_u64 v[72:73], s[20:21], 0, v[202:203]
	v_lshl_add_u64 v[74:75], s[22:23], 0, v[204:205]
	v_mfma_f32_16x16x32_bf16 v[24:27], v[134:137], v[114:117], v[24:27]
	v_mfma_f32_16x16x32_bf16 v[20:23], v[134:137], v[106:109], v[20:23]
	s_waitcnt vmcnt(0)
	v_mfma_f32_16x16x32_bf16 v[8:11], v[134:137], v[138:141], v[8:11]
	s_cbranch_vccnz .LBB0_539
; __device__ __forceinline__ unsigned hg_pk(float lo, float hi) { unsigned r; asm volatile("v_cvt_pk_bf16_f32 %0, %1, %2" : "=v"(r) : "v"(lo), "v"(hi)); return r; }
; #define HG_SB() __builtin_amdgcn_sched_barrier(0)
; __device__ __forceinline__ void ph_hgrn_out2(const P& p, int l, int jmin, int gw, int nw, int lane) {
;     ...
;       for (int J = 0; J < 4; ++J) {
;         if (dir == 0 ? (J <= I) : (J >= I)) {
;           const int rowk = rbase + 16 * J + r16; f32x4 T = {0.f, 0.f, 0.f, 0.f};
;           f32x4 kb[4][2]; u32x4 kw[4];
;           HG_SB();
; #pragma unroll
;           for (int ks = 0; ks < 4; ++ks) { kb[ks][0] = *(const f32x4*)(BC + (size_t)rowk * 1024 + colb + 32 * ks); kb[ks][1] = *(const f32x4*)(BC + (size_t)rowk * 1024 + colb + 32 * ks + 4);
;             kw[ks] = *(const u32x4*)(KM + (size_t)rowk * 1024 + colb + 32 * ks); }
;           HG_SB();
; #pragma unroll
;           for (int ks = 0; ks < 4; ++ks) { u32x4 fw;
; #pragma unroll
;             for (int jj = 0; jj < 4; ++jj) { const float ka = __uint_as_float(kw[ks][jj] << 16), kbb = __uint_as_float(kw[ks][jj] & 0xffff0000u);
;               const float ba = jj < 2 ? kb[ks][0][2 * jj] : kb[ks][1][2 * jj - 4], bb = jj < 2 ? kb[ks][0][2 * jj + 1] : kb[ks][1][2 * jj - 3];
;               fw[jj] = hg_pk(ka * __expf(fminf(refv[ks][2 * jj] - ba, 80.f)), kbb * __expf(fminf(refv[ks][2 * jj + 1] - bb, 80.f))); }
;             T = __builtin_amdgcn_mfma_f32_16x16x32_bf16(__builtin_bit_cast(hg_bf16x8, fw), Qs[ks], T, 0, 0, 0); }
	v_lshl_add_u64 v[64:65], v[194:195], 2, v[72:73]
	v_lshl_add_u64 v[66:67], v[194:195], 1, v[74:75]
	global_load_dwordx4 v[76:79], v[64:65], off offset:16
	global_load_dwordx4 v[80:83], v[64:65], off
	global_load_dwordx4 v[84:87], v[64:65], off offset:144
	global_load_dwordx4 v[88:91], v[64:65], off offset:128
	global_load_dwordx4 v[98:101], v[66:67], off
	global_load_dwordx4 v[102:105], v[66:67], off offset:64
	global_load_dwordx4 v[106:109], v[64:65], off offset:272
	global_load_dwordx4 v[110:113], v[64:65], off offset:256
	global_load_dwordx4 v[68:71], v[64:65], off offset:400
	global_load_dwordx4 v[114:117], v[64:65], off offset:384
	global_load_dwordx4 v[118:121], v[66:67], off offset:128
	s_nop 0
	global_load_dwordx4 v[64:67], v[66:67], off offset:192
	s_waitcnt vmcnt(10)
	v_sub_f32_e32 v80, v222, v80
	v_sub_f32_e32 v81, v221, v81
	v_min_f32_e32 v80, 0x42a00000, v80
	v_min_f32_e32 v81, 0x42a00000, v81
	v_mul_f32_e32 v80, 0x3fb8aa3b, v80
	v_mul_f32_e32 v81, 0x3fb8aa3b, v81
	v_exp_f32_e32 v80, v80
	v_exp_f32_e32 v81, v81
	s_waitcnt vmcnt(7)
	v_lshlrev_b32_e32 v92, 16, v98
	v_and_b32_e32 v93, 0xffff0000, v98
	v_mul_f32_e32 v80, v80, v92
	v_mul_f32_e32 v81, v81, v93
	v_cvt_pk_bf16_f32 v80, v80, v81
	v_sub_f32_e32 v81, v211, v82
	v_sub_f32_e32 v82, v210, v83
	v_min_f32_e32 v81, 0x42a00000, v81
	v_min_f32_e32 v82, 0x42a00000, v82
	v_mul_f32_e32 v81, 0x3fb8aa3b, v81
	v_mul_f32_e32 v82, 0x3fb8aa3b, v82
	v_sub_f32_e32 v76, v189, v76
	v_sub_f32_e32 v77, v177, v77
	v_exp_f32_e32 v81, v81
	v_exp_f32_e32 v82, v82
	v_min_f32_e32 v76, 0x42a00000, v76
	v_min_f32_e32 v77, 0x42a00000, v77
	v_mul_f32_e32 v76, 0x3fb8aa3b, v76
	v_mul_f32_e32 v77, 0x3fb8aa3b, v77
	v_exp_f32_e32 v76, v76
	v_exp_f32_e32 v77, v77
	v_lshlrev_b32_e32 v83, 16, v99
	v_and_b32_e32 v92, 0xffff0000, v99
	v_mul_f32_e32 v81, v81, v83
	v_mul_f32_e32 v82, v82, v92
	v_cvt_pk_bf16_f32 v81, v81, v82
	v_lshlrev_b32_e32 v82, 16, v100
	v_and_b32_e32 v83, 0xffff0000, v100
	v_mul_f32_e32 v76, v76, v82
	v_mul_f32_e32 v77, v77, v83
	v_cvt_pk_bf16_f32 v82, v76, v77
	v_sub_f32_e32 v76, v96, v78
	v_sub_f32_e32 v77, v175, v79
	v_min_f32_e32 v76, 0x42a00000, v76
	v_min_f32_e32 v77, 0x42a00000, v77
	v_mul_f32_e32 v76, 0x3fb8aa3b, v76
	v_mul_f32_e32 v77, 0x3fb8aa3b, v77
	v_exp_f32_e32 v76, v76
	v_exp_f32_e32 v77, v77
	v_lshlrev_b32_e32 v78, 16, v101
	v_and_b32_e32 v79, 0xffff0000, v101
	v_mul_f32_e32 v76, v76, v78
	v_mul_f32_e32 v77, v77, v79
	v_cvt_pk_bf16_f32 v83, v76, v77
	s_waitcnt vmcnt(3)
	v_sub_f32_e32 v68, v162, v68
	v_mfma_f32_16x16x32_bf16 v[76:79], v[80:83], v[48:51], 0
	v_sub_f32_e32 v80, v230, v88
	v_sub_f32_e32 v81, v229, v89
	v_min_f32_e32 v80, 0x42a00000, v80
	v_min_f32_e32 v81, 0x42a00000, v81
	v_mul_f32_e32 v80, 0x3fb8aa3b, v80
	v_mul_f32_e32 v81, 0x3fb8aa3b, v81
	v_exp_f32_e32 v80, v80
	v_exp_f32_e32 v81, v81
	v_lshlrev_b32_e32 v82, 16, v102
	v_and_b32_e32 v83, 0xffff0000, v102
	v_mul_f32_e32 v80, v80, v82
	v_mul_f32_e32 v81, v81, v83
	v_cvt_pk_bf16_f32 v80, v80, v81
	v_sub_f32_e32 v81, v228, v90
	v_sub_f32_e32 v82, v227, v91
	v_min_f32_e32 v81, 0x42a00000, v81
	v_min_f32_e32 v82, 0x42a00000, v82
	v_mul_f32_e32 v81, 0x3fb8aa3b, v81
	v_mul_f32_e32 v82, 0x3fb8aa3b, v82
	v_exp_f32_e32 v81, v81
	v_exp_f32_e32 v82, v82
	v_lshlrev_b32_e32 v83, 16, v103
	v_and_b32_e32 v88, 0xffff0000, v103
	v_mul_f32_e32 v81, v81, v83
	v_mul_f32_e32 v82, v82, v88
	v_cvt_pk_bf16_f32 v81, v81, v82
	v_sub_f32_e32 v82, v226, v84
	v_sub_f32_e32 v83, v225, v85
	v_min_f32_e32 v82, 0x42a00000, v82
	v_min_f32_e32 v83, 0x42a00000, v83
	v_mul_f32_e32 v82, 0x3fb8aa3b, v82
	v_mul_f32_e32 v83, 0x3fb8aa3b, v83
	v_exp_f32_e32 v82, v82
	v_exp_f32_e32 v83, v83
	v_lshlrev_b32_e32 v84, 16, v104
	v_and_b32_e32 v85, 0xffff0000, v104
	v_mul_f32_e32 v82, v82, v84
	v_mul_f32_e32 v83, v83, v85
	v_cvt_pk_bf16_f32 v82, v82, v83
	v_sub_f32_e32 v83, v223, v86
	v_min_f32_e32 v83, 0x42a00000, v83
	v_sub_f32_e32 v84, v224, v87
	v_mul_f32_e32 v83, 0x3fb8aa3b, v83
	v_min_f32_e32 v84, 0x42a00000, v84
	v_exp_f32_e32 v83, v83
	v_mul_f32_e32 v84, 0x3fb8aa3b, v84
	v_exp_f32_e32 v84, v84
	v_lshlrev_b32_e32 v85, 16, v105
	v_and_b32_e32 v86, 0xffff0000, v105
	v_mul_f32_e32 v83, v83, v85
	v_mul_f32_e32 v84, v84, v86
	v_cvt_pk_bf16_f32 v83, v83, v84
	s_waitcnt vmcnt(1)
; __device__ __forceinline__ unsigned hg_pk(float lo, float hi) { unsigned r; asm volatile("v_cvt_pk_bf16_f32 %0, %1, %2" : "=v"(r) : "v"(lo), "v"(hi)); return r; }
; __device__ __forceinline__ void ph_hgrn_out2(const P& p, int l, int jmin, int gw, int nw, int lane) {
;     ...
;           for (int ks = 0; ks < 4; ++ks) { u32x4 fw;
; #pragma unroll
;             for (int jj = 0; jj < 4; ++jj) { const float ka = __uint_as_float(kw[ks][jj] << 16), kbb = __uint_as_float(kw[ks][jj] & 0xffff0000u);
;               const float ba = jj < 2 ? kb[ks][0][2 * jj] : kb[ks][1][2 * jj - 4], bb = jj < 2 ? kb[ks][0][2 * jj + 1] : kb[ks][1][2 * jj - 3];
;               fw[jj] = hg_pk(ka * __expf(fminf(refv[ks][2 * jj] - ba, 80.f)), kbb * __expf(fminf(refv[ks][2 * jj + 1] - bb, 80.f))); }
;             T = __builtin_amdgcn_mfma_f32_16x16x32_bf16(__builtin_bit_cast(hg_bf16x8, fw), Qs[ks], T, 0, 0, 0); }
;           if (J == I) {
; #pragma unroll
;             for (int rg = 0; rg < 4; ++rg) { const int sl = 4 * q + rg; const bool keep = dir == 0 ? (sl <= r16) : (sl >= r16); T[rg] = keep ? T[rg] : 0.f; } }
;           AT[J] += T;
	v_and_b32_e32 v84, 0xffff0000, v119
	v_mfma_f32_16x16x32_bf16 v[76:79], v[80:83], v[52:55], v[76:79]
	v_sub_f32_e32 v80, v233, v110
	v_sub_f32_e32 v81, v232, v111
	v_min_f32_e32 v80, 0x42a00000, v80
	v_min_f32_e32 v81, 0x42a00000, v81
	v_mul_f32_e32 v80, 0x3fb8aa3b, v80
	v_mul_f32_e32 v81, 0x3fb8aa3b, v81
	v_exp_f32_e32 v80, v80
	v_exp_f32_e32 v81, v81
	v_lshlrev_b32_e32 v82, 16, v118
	v_and_b32_e32 v83, 0xffff0000, v118
	v_mul_f32_e32 v80, v80, v82
	v_mul_f32_e32 v81, v81, v83
	v_cvt_pk_bf16_f32 v80, v80, v81
	v_sub_f32_e32 v81, v171, v112
	v_sub_f32_e32 v82, v168, v113
	v_min_f32_e32 v81, 0x42a00000, v81
	v_min_f32_e32 v82, 0x42a00000, v82
	v_mul_f32_e32 v81, 0x3fb8aa3b, v81
	v_mul_f32_e32 v82, 0x3fb8aa3b, v82
	v_exp_f32_e32 v81, v81
	v_exp_f32_e32 v82, v82
	v_lshlrev_b32_e32 v83, 16, v119
	v_and_b32_e32 v85, 0xffff0000, v120
	v_mul_f32_e32 v81, v81, v83
	v_mul_f32_e32 v82, v82, v84
	v_cvt_pk_bf16_f32 v81, v81, v82
	v_sub_f32_e32 v82, v231, v106
	v_sub_f32_e32 v83, v170, v107
	v_min_f32_e32 v82, 0x42a00000, v82
	v_min_f32_e32 v83, 0x42a00000, v83
	v_mul_f32_e32 v82, 0x3fb8aa3b, v82
	v_mul_f32_e32 v83, 0x3fb8aa3b, v83
	v_exp_f32_e32 v82, v82
	v_exp_f32_e32 v83, v83
	v_lshlrev_b32_e32 v84, 16, v120
	v_and_b32_e32 v86, 0xffff0000, v121
	v_mul_f32_e32 v82, v82, v84
	v_mul_f32_e32 v83, v83, v85
	v_cvt_pk_bf16_f32 v82, v82, v83
	v_sub_f32_e32 v83, v166, v108
	v_min_f32_e32 v83, 0x42a00000, v83
	v_sub_f32_e32 v84, v167, v109
	v_mul_f32_e32 v83, 0x3fb8aa3b, v83
	v_min_f32_e32 v84, 0x42a00000, v84
	v_exp_f32_e32 v83, v83
	v_mul_f32_e32 v84, 0x3fb8aa3b, v84
	v_exp_f32_e32 v84, v84
	v_lshlrev_b32_e32 v85, 16, v121
	v_mul_f32_e32 v83, v83, v85
	v_sub_f32_e32 v69, v150, v69
	v_mul_f32_e32 v84, v84, v86
	v_cvt_pk_bf16_f32 v83, v83, v84
	v_min_f32_e32 v68, 0x42a00000, v68
	v_mfma_f32_16x16x32_bf16 v[76:79], v[80:83], v[56:59], v[76:79]
	v_sub_f32_e32 v80, v164, v114
	v_sub_f32_e32 v81, v163, v115
	v_min_f32_e32 v80, 0x42a00000, v80
	v_min_f32_e32 v81, 0x42a00000, v81
	v_mul_f32_e32 v80, 0x3fb8aa3b, v80
	v_mul_f32_e32 v81, 0x3fb8aa3b, v81
	v_exp_f32_e32 v80, v80
	v_exp_f32_e32 v81, v81
	s_waitcnt vmcnt(0)
	v_lshlrev_b32_e32 v82, 16, v64
	v_and_b32_e32 v64, 0xffff0000, v64
	v_mul_f32_e32 v80, v80, v82
	v_mul_f32_e32 v64, v81, v64
	v_cvt_pk_bf16_f32 v64, v80, v64
	v_sub_f32_e32 v80, v151, v116
	v_sub_f32_e32 v81, v148, v117
	v_min_f32_e32 v80, 0x42a00000, v80
	v_min_f32_e32 v81, 0x42a00000, v81
	v_mul_f32_e32 v80, 0x3fb8aa3b, v80
	v_mul_f32_e32 v81, 0x3fb8aa3b, v81
	v_exp_f32_e32 v80, v80
	v_exp_f32_e32 v81, v81
	v_min_f32_e32 v69, 0x42a00000, v69
	v_mul_f32_e32 v68, 0x3fb8aa3b, v68
	v_mul_f32_e32 v69, 0x3fb8aa3b, v69
	v_exp_f32_e32 v68, v68
	v_exp_f32_e32 v69, v69
	v_lshlrev_b32_e32 v82, 16, v65
	v_and_b32_e32 v65, 0xffff0000, v65
	v_mul_f32_e32 v80, v80, v82
	v_mul_f32_e32 v65, v81, v65
	v_cvt_pk_bf16_f32 v65, v80, v65
	v_lshlrev_b32_e32 v80, 16, v66
	v_and_b32_e32 v66, 0xffff0000, v66
	v_mul_f32_e32 v68, v68, v80
	v_mul_f32_e32 v66, v69, v66
	v_sub_f32_e32 v69, v147, v71
	v_cvt_pk_bf16_f32 v66, v68, v66
	v_sub_f32_e32 v68, v146, v70
	v_min_f32_e32 v69, 0x42a00000, v69
	v_min_f32_e32 v68, 0x42a00000, v68
	v_mul_f32_e32 v69, 0x3fb8aa3b, v69
	v_mul_f32_e32 v68, 0x3fb8aa3b, v68
	v_exp_f32_e32 v69, v69
	v_exp_f32_e32 v68, v68
	v_lshlrev_b32_e32 v70, 16, v67
	v_and_b32_e32 v67, 0xffff0000, v67
	v_mul_f32_e32 v67, v69, v67
	v_mul_f32_e32 v68, v68, v70
	v_cvt_pk_bf16_f32 v67, v68, v67
	s_andn2_b64 vcc, exec, s[74:75]
	v_mfma_f32_16x16x32_bf16 v[64:67], v[64:67], v[60:63], v[76:79]
	s_mov_b64 s[6:7], -1
	s_cbranch_vccnz .LBB0_536
	s_mov_b64 s[6:7], 0

; #define PG8_STAGE(bufoff, gbase, voff) do { _Pragma("unroll") for (int _i = 0; _i < 2; ++_i) \
;         __builtin_amdgcn_global_load_lds((const unsigned*)((const char*)(gbase) + (voff)[_i]), (LAS unsigned*)(lds + (bufoff) + ldsw + _i * 8192), 16, 0, 0); } while (0)
; #define PG8_WAIT_V(n) asm volatile("s_waitcnt vmcnt(" #n ")" ::: "memory")
; #define PG8_BAR __builtin_amdgcn_s_barrier()
; template <class Epi, class Sched, bool GATHER, bool ALIGN_EPI>
; __device__ __forceinline__ void gemm_phase(LAS unsigned char* lds, const int K, const Sched& S, const Epi& E, const int* tokmap, int wave_id) {
;     unsigned z_ = 0u; asm volatile("" : "+v"(z_)); int tid = wave_id * 64 + (int)__builtin_amdgcn_mbcnt_hi(~0u, __builtin_amdgcn_mbcnt_lo(~0u, z_)); asm volatile("" : "+v"(tid));
;     const int wid = __builtin_amdgcn_readfirstlane(tid >> 6), lane = tid & 63, wr = wid >> 2, wc = wid & 3, fr = lane & 15, fq = lane >> 4;
;     const int nt = K / BK;
;     int sR[2], sC[2]; unsigned voffB[2];
; #pragma unroll
;     for (int i = 0; i < 2; ++i) { int R, C; stage_rc(tid * 16 + i * 8192, R, C); sR[i] = R; sC[i] = C; const int Rb = (R & ~31) + perm32(R & 31); voffB[i] = (unsigned)(Rb * K + C) * 2u; }
;     const size_t kstep = (size_t)(BK * 2);
;     const size_t hstep = (size_t)HALF * K * 2;
;     const unsigned ldsw = (unsigned)wid * 1024u;
;     const int aoff = lds_byte(wr * 64 + fr, fq * 8), boff = lds_byte(wc * 32 + fr, fq * 8);
;     ...
;     Unit cur, nxt; int ui = 0;
;     if (!S.next(0, cur)) return;
;     f32x4 acc[2][2][4][2];
; #pragma unroll
;     for (int a = 0; a < 2; ++a)
; #pragma unroll
;         for (int b = 0; b < 2; ++b)
; #pragma unroll
;             for (int m = 0; m < 4; ++m)
; #pragma unroll
;                 for (int n = 0; n < 2; ++n) acc[a][b][m][n] = (f32x4){0.f, 0.f, 0.f, 0.f};
;     bf16x8 At[4][2], B0[2][2], B1[2][2];
;     unsigned vA[2][2], vN[2][2];
;     PG8_MKV(vA, cur);
;     const char* cA = S.a_ptr(cur); const char* cB = S.b_ptr(cur);
;     PG8_STAGE(PG8_SB(0, 0), cB, voffB); PG8_STAGE(PG8_SB(0, 1), cB + hstep, voffB); PG8_STAGE(PG8_SA(0, 0), cA, vA[0]); PG8_STAGE(PG8_SA(0, 1), cA, vA[1]);
;     if (wr == 1) PG8_BAR;
;     PG8_WAIT_V(2); PG8_BAR;
;     PG8_STAGE(PG8_SB(1, 0), cB + kstep, voffB); PG8_STAGE(PG8_SA(1, 0), cA + kstep, vA[0]); PG8_STAGE(PG8_SB(1, 1), cB + hstep + kstep, voffB);
.LBB0_1124:
	s_load_dwordx2 s[0:1], s[6:7], 0xc8
	s_load_dwordx4 s[44:47], s[6:7], 0x40
	s_load_dwordx4 s[48:51], s[6:7], 0xb8
	s_and_b64 vcc, exec, s[18:19]
	s_cbranch_vccz .LBB0_1154
	s_cmp_ge_i32 s9, s14
	s_cbranch_scc1 .LBB0_1154
	v_bfe_i32 v2, v4, 27, 1
	v_lshlrev_b32_e32 v0, 4, v4
	v_lshrrev_b32_e32 v2, 22, v2
	v_add_u32_e32 v2, v0, v2
	v_and_b32_e32 v2, 0xfffffc00, v2
	v_sub_u32_e32 v2, v0, v2
	v_ashrrev_i32_e32 v1, 31, v4
	v_lshrrev_b32_e32 v3, 4, v2
	v_lshrrev_b32_e32 v1, 26, v1
	v_bitop3_b32 v2, v3, v2, 32 bitop3:0x6c
	v_add_u32_e32 v1, v4, v1
	v_ashrrev_i32_e32 v5, 31, v2
	v_ashrrev_i32_e32 v1, 6, v1
	v_lshrrev_b32_e32 v5, 26, v5
	v_lshlrev_b32_e32 v3, 3, v1
	v_add_u32_e32 v5, v2, v5
	v_and_b32_e32 v3, -16, v3
	v_ashrrev_i32_e32 v6, 6, v5
	s_add_u32 s18, s12, 0x205b4000
	v_add_u32_e32 v147, v6, v3
	v_and_b32_e32 v3, 0xc0, v5
	s_addc_u32 s19, s13, 0
	s_lshl_b64 s[6:7], s[78:79], 27
	v_sub_u32_e32 v2, v2, v3
	s_add_u32 s5, s70, s6
	v_lshlrev_b32_e32 v1, 5, v1
	v_ashrrev_i16_sdwa v2, v219, sext(v2) dst_sel:DWORD dst_unused:UNUSED_PAD src0_sel:DWORD src1_sel:BYTE_0
	s_addc_u32 s72, s71, s7
	s_lshl_b32 s6, s78, 7
	v_and_b32_e32 v1, 32, v1
	v_bfe_i32 v2, v2, 0, 16
	v_add_u32_e32 v0, 0x2000, v0
	s_ashr_i32 s7, s6, 31
	v_add_lshl_u32 v148, v1, v2, 1
	v_ashrrev_i32_e32 v1, 31, v0
	s_mov_b32 s4, s78
	s_lshl_b64 s[6:7], s[6:7], 2
	v_lshrrev_b32_e32 v1, 22, v1
	v_writelane_b32 v255, s4, 23
	s_add_u32 s3, s12, s6
	v_add_u32_e32 v1, v0, v1
	v_writelane_b32 v255, s5, 24
	s_addc_u32 s4, s13, s7
	v_ashrrev_i32_e32 v1, 10, v1
	s_add_u32 s73, s3, 0x1600
	v_mul_i32_i24_e32 v2, 0x400, v1
	s_addc_u32 s74, s4, 0
	v_lshlrev_b32_e32 v3, 1, v147
	v_lshrrev_b32_e32 v5, 2, v147
	v_and_b32_e32 v6, 3, v6
	s_mov_b32 s4, 0xfffe0
	v_sub_u32_e32 v0, v0, v2
	v_and_b32_e32 v3, 24, v3
	v_and_b32_e32 v5, 4, v5
	v_and_or_b32 v6, v147, s4, v6
	v_lshrrev_b32_e32 v2, 4, v0
	v_or3_b32 v3, v6, v5, v3
	v_bitop3_b32 v0, v2, v0, 32 bitop3:0x6c
	v_lshl_add_u32 v130, v3, 12, v148
	v_ashrrev_i32_e32 v3, 31, v0
	v_lshrrev_b32_e32 v3, 26, v3
	s_add_u32 s20, s12, 0x33b45800
	v_lshlrev_b32_e32 v2, 3, v1
	v_add_u32_e32 v3, v0, v3
	s_addc_u32 s21, s13, 0
	v_and_b32_e32 v2, -16, v2
	v_ashrrev_i32_e32 v5, 6, v3
	s_ashr_i32 s6, s9, 31
	v_add_u32_e32 v149, v5, v2
	v_and_b32_e32 v2, 0xc0, v3
	s_lshr_b32 s6, s6, 30
	v_sub_u32_e32 v0, v0, v2
	s_add_i32 s6, s9, s6
	v_lshlrev_b32_e32 v1, 5, v1
	v_ashrrev_i16_sdwa v0, v219, sext(v0) dst_sel:DWORD dst_unused:UNUSED_PAD src0_sel:DWORD src1_sel:BYTE_0
	s_ashr_i32 s38, s6, 2
	s_and_b32 s6, s6, -4
	v_and_b32_e32 v1, 32, v1
	v_bfe_i32 v0, v0, 0, 16
	s_sub_i32 s62, s9, s6
	s_lshl_b32 s6, s38, 8
	v_add_lshl_u32 v150, v1, v0, 1
	v_add_u32_e32 v0, s6, v147
	v_ashrrev_i32_e32 v1, 31, v0
	v_lshl_add_u64 v[0:1], v[0:1], 2, s[20:21]
	global_load_dword v6, v[0:1], off
	v_add_u32_e32 v0, s6, v149
	v_ashrrev_i32_e32 v1, 31, v0
	v_lshl_add_u64 v[0:1], v[0:1], 2, s[20:21]
	global_load_dword v7, v[0:1], off
	v_and_b32_e32 v5, 3, v5
	v_and_or_b32 v5, v149, s4, v5
	s_ashr_i32 s4, s2, 6
	s_ashr_i32 s39, s38, 31
	s_ashr_i32 s3, s2, 8
	s_lshl_b32 s75, s4, 10
	s_ashr_i32 s63, s62, 31
	v_lshlrev_b32_e32 v2, 1, v149
	v_lshrrev_b32_e32 v3, 2, v149
	v_and_b32_e32 v2, 24, v2
	v_and_b32_e32 v3, 4, v3
	v_or3_b32 v2, v5, v3, v2
	v_lshl_add_u32 v132, v2, 12, v150
	v_mov_b32_e32 v131, v97
	v_mov_b32_e32 v133, v97
	s_bitset1_b32 s6, 7
	v_add_u32_e32 v0, s6, v147
	v_ashrrev_i32_e32 v1, 31, v0
	v_lshl_add_u64 v[0:1], v[0:1], 2, s[20:21]
	global_load_dword v8, v[0:1], off
	v_add_u32_e32 v0, s6, v149
	v_ashrrev_i32_e32 v1, 31, v0
	v_lshl_add_u64 v[0:1], v[0:1], 2, s[20:21]
	global_load_dword v9, v[0:1], off
	s_lshl_b64 s[6:7], s[38:39], 2
	s_add_u32 s6, s73, s6
	s_addc_u32 s7, s74, s7
	global_load_dword v0, v97, s[6:7]
	s_waitcnt vmcnt(0)
	v_max_i32_e32 v6, 0, v6
	v_lshl_add_u32 v134, v6, 12, v148
	v_max_i32_e32 v7, 0, v7
	v_lshl_add_u32 v136, v7, 12, v150
	v_max_i32_e32 v8, 0, v8
	v_lshl_add_u32 v138, v8, 12, v148
	v_max_i32_e32 v9, 0, v9
	v_lshl_add_u32 v140, v9, 12, v150
	v_readfirstlane_b32 s64, v0
	s_lshl_b64 s[6:7], s[64:65], 22
	s_add_u32 s9, s5, s6
	s_addc_u32 s16, s72, s7
	s_lshl_b64 s[6:7], s[62:63], 20
	s_add_u32 s66, s9, s6
	s_addc_u32 s67, s16, s7
	s_add_i32 s39, s75, 0
	s_add_i32 m0, s39, 0x10000
	v_lshl_add_u64 v[0:1], s[66:67], 0, v[130:131]
	global_load_lds_dwordx4 v130, s[66:67]
	s_add_i32 m0, s39, 0x12000
	s_add_u32 s6, s66, 0x80000
	global_load_lds_dwordx4 v132, s[66:67]
	s_addc_u32 s7, s67, 0
	s_add_i32 m0, s39, 0x14000
	s_add_i32 s63, s39, 0x2000
	global_load_lds_dwordx4 v130, s[6:7]
	s_add_i32 m0, s39, 0x16000
	s_add_i32 s76, s39, 0x4000
	global_load_lds_dwordx4 v132, s[6:7]
	s_mov_b32 m0, s39
	s_add_i32 s77, s39, 0x6000
	global_load_lds_dwordx4 v134, s[18:19]
	s_mov_b32 m0, s63
	s_cmp_eq_u32 s3, 1
	global_load_lds_dwordx4 v136, s[18:19]
	s_mov_b32 m0, s76
	v_lshl_add_u64 v[2:3], s[66:67], 0, v[132:133]
	global_load_lds_dwordx4 v138, s[18:19]
	s_mov_b32 m0, s77
	s_cselect_b64 s[22:23], -1, 0
	global_load_lds_dwordx4 v140, s[18:19]
	s_cmp_lg_u32 s3, 1
	s_cbranch_scc1 .LBB0_1128
	s_barrier
